# P5 residual epilogue rewritten (all f32 base rows of a unit requested up front) and 768 conversion items moved from the P5 side workgroups to the P8/P9 tails
# speedup vs baseline: 1.0136x; 1.0136x over previous
; #define LAS __attribute__((address_space(3)))
; #define SIDE_CVT(GA, LO, HI) do { CVT_MKCP(); cvt_range(CP, LO, HI, (bid - (GA)) * 8 + wave, (G - (GA)) * 8, cscr, lane); } while (0)
; #define PHASE(k) if (IN(k)) _Pragma("unroll") for (int rep_ = 0; rep_ < 1 + (int)((DUP_MASK >> (k)) & 1u); ++rep_)
; #define REP_BAR() do { if (rep_) GRID_BAR(); } while (0)
; DI void cvt_range(const CvtPtrs& P, int lo, int hi, int w, int NW, LAS unsigned* scr, int lane) {
;     int it = lo + w; if (it >= hi) return;
;     const int c = lane & 15, q = lane >> 4;
;     const float* src; int ldw; bf16_t* dst; int ldd; bool qperm, f8; cvt_resolve(P, it, src, ldw, dst, ldd, qperm, f8);
; __global__ void __launch_bounds__(512, 2) dit_fwd(Args args) {
;     ...
;     PHASE(5) { REP_BAR();
;         if (bid < GA45) {
;         pg8::Gemm g{Z, W2, MT, DM, DM}; pg8::StaticOrder S; S.init(MT, DM, GA45, bid);
;         EpiResid<true> E{x, ctx, H, mod + 2 * DM, 1.0f};
;         pg8::gemm_phase<EpiResid<true>, pg8::StaticOrder, true, true>(lds, g, S, E);
;         } else SIDE_CVT(GA45, C4, C5);
.LBB0_444:
	v_readlane_b32 s4, v251, 0
	v_readlane_b32 s5, v251, 1
	s_cmp_lt_i32 s4, 6
	s_cselect_b64 s[4:5], -1, 0
	s_add_u32 s92, s82, 0x1c800000
	s_addc_u32 s93, s83, 0
	s_and_b64 s[6:7], s[4:5], s[0:1]
	s_andn2_b64 vcc, exec, s[6:7]
	s_cbranch_vccnz .LBB0_501
	v_lshlrev_b32_e32 v103, 4, v0
	s_cmp_ge_i32 s2, s68
	v_lshlrev_b32_e32 v1, 2, v0
	v_lshrrev_b32_e32 v137, 1, v0
	v_and_b32_e32 v98, 48, v103
	s_mov_b64 s[0:1], -1
	s_cbranch_scc0 .LBB0_484
	s_sub_i32 s0, s2, s68
	s_lshl_b32 s0, s0, 3
	v_readlane_b32 s1, v251, 25
	s_add_i32 s0, s0, s1
	s_cmpk_gt_u32 s0, 0x347f
	s_cbranch_scc1 .LBB0_483
	s_sub_i32 s1, s33, s68
	s_lshl_b32 s26, s1, 3
	s_cmpk_lt_u32 s0, 0xe00
	s_movk_i32 s1, 0x5200
	s_cselect_b32 s1, s1, 0xfffff200
	s_add_i32 s1, s1, s0
	s_cmpk_gt_u32 s0, 0xdff
	s_cselect_b32 s4, 16, 0
	s_bfe_u32 s5, s1, 0x40009
	s_or_b32 s8, s5, s4
	s_cmpk_lt_u32 s1, 0x4000
	s_cselect_b64 s[4:5], -1, 0
	s_lshr_b32 s9, s0, 5
	s_bfe_u32 s27, s88, 0x30006
	s_and_b32 s9, s9, 8
	v_readlane_b32 s16, v251, 28
	s_or_b32 s9, s9, s27
	s_lshl_b32 s10, s8, 23
	v_readlane_b32 s22, v251, 34
	v_readlane_b32 s23, v251, 35
	s_add_u32 s11, s22, s10
	s_addc_u32 s14, s23, 0
	s_lshl_b32 s15, s9, 6
	s_lshl_b32 s9, s9, 19
	s_add_u32 s9, s11, s9
	s_addc_u32 s11, s14, 0
	s_lshl_b32 s14, s1, 3
	v_readlane_b32 s17, v251, 29
	s_and_b32 s16, s14, 0x7c0
	s_lshl_b32 s17, s16, 2
	s_add_u32 s17, s9, s17
	s_addc_u32 s9, s11, 0
	s_lshr_b32 s0, s0, 4
	s_lshl_b32 s11, s8, 21
	s_lshl_b32 s16, s16, 10
	s_and_b32 s0, s0, 24
	s_or_b32 s11, s11, s16
	s_or_b32 s0, s0, s27
	v_readlane_b32 s18, v251, 30
	v_readlane_b32 s20, v251, 32
	s_cmpk_lt_u32 s1, 0x2000
	v_readlane_b32 s19, v251, 31
	v_readlane_b32 s21, v251, 33
	s_cselect_b32 s18, s18, s20
	s_cselect_b32 s16, s19, s21
	s_add_u32 s10, s18, s10
	s_addc_u32 s16, s16, 0
	s_lshl_b32 s18, s0, 6
	s_lshl_b32 s0, s0, 18
	s_add_u32 s0, s10, s0
	s_addc_u32 s10, s16, 0
	s_lshl_b32 s16, s1, 5
	s_and_b32 s16, s16, 0xf00
	s_add_u32 s16, s0, s16
	s_addc_u32 s10, s10, 0
	s_lshl_b32 s0, s8, 11
	s_lshl_b32 s8, s1, 4
	s_and_b32 s8, s8, 0x700
	s_lshr_b32 s1, s1, 6
	s_or_b32 s0, s0, s8
	s_and_b32 s1, s1, 0x80
	s_or_b32 s0, s0, s1
	s_and_b32 s1, s14, 64
	s_or_b32 s0, s0, s1
	s_lshl_b32 s8, s0, 11
	s_and_b64 s[0:1], s[4:5], exec
	s_cselect_b32 s0, s8, s11
	v_readlane_b32 s1, v250, 8
	v_readlane_b32 s8, v250, 11
	s_cselect_b32 s1, s1, s8
	v_readlane_b32 s8, v250, 7
	v_readlane_b32 s11, v250, 10
	s_cselect_b32 s11, s8, s11
	s_cselect_b32 s9, s10, s9
	s_movk_i32 s10, 0x800
	s_cselect_b32 s14, 0, 0
	s_cselect_b32 s15, s18, s15
	s_cselect_b32 s8, s16, s17
	s_cselect_b32 s28, s10, 0x400
	s_add_u32 s0, s11, s0
	s_addc_u32 s1, s1, 0
	s_add_u32 s0, s0, s15
	s_addc_u32 s1, s1, s14
	v_and_b32_e32 v102, 60, v1
	v_mov_b32_e32 v105, 0
	s_and_b64 s[4:5], s[4:5], exec
	v_and_b32_e32 v100, 48, v0
	v_mov_b32_e32 v101, v105
	v_lshlrev_b32_e32 v104, 2, v102
	s_cselect_b32 s4, 10, 11
	v_or_b32_e32 v106, 1, v100
	v_mov_b32_e32 v107, v105
	s_waitcnt vmcnt(0) lgkmcnt(0)
; #define LDS_WAIT() asm volatile("s_waitcnt lgkmcnt(0)" ::: "memory")
; DI unsigned pk2(float lo, float hi) { return cvt_pk_bf16(lo, hi); }
; DI void cvt_range(const CvtPtrs& P, int lo, int hi, int w, int NW, LAS unsigned* scr, int lane) {
;     ...
;     for (int rr = 0; rr < 16; ++rr) v[rr] = __builtin_nontemporal_load((const f32x4*)(src + (size_t)(16 * q + rr) * ldw + 4 * c));
;     for (;;) {
;         const bool cf8 = f8; const int wrow = qperm ? 32 * ((c >> 2) & 1) + 8 * (c & 3) + 4 * (c >> 3) : 4 * c;
;         u32x4 pa[4], pb[4];
;         if (cf8) {
; #pragma unroll
;             for (int i = 0; i < 4; ++i) { pa[i].x = pk4_fp8(v[0][i] * W8_SCALE, v[1][i] * W8_SCALE, v[2][i] * W8_SCALE, v[3][i] * W8_SCALE); pa[i].y = pk4_fp8(v[4][i] * W8_SCALE, v[5][i] * W8_SCALE, v[6][i] * W8_SCALE, v[7][i] * W8_SCALE);
;                                           pa[i].z = pk4_fp8(v[8][i] * W8_SCALE, v[9][i] * W8_SCALE, v[10][i] * W8_SCALE, v[11][i] * W8_SCALE); pa[i].w = pk4_fp8(v[12][i] * W8_SCALE, v[13][i] * W8_SCALE, v[14][i] * W8_SCALE, v[15][i] * W8_SCALE); pb[i] = pa[i]; }
;         } else {
; #pragma unroll
;             for (int i = 0; i < 4; ++i) { pa[i].x = pk2(v[0][i], v[1][i]); pa[i].y = pk2(v[2][i], v[3][i]); pa[i].z = pk2(v[4][i], v[5][i]); pa[i].w = pk2(v[6][i], v[7][i]);
;                                           pb[i].x = pk2(v[8][i], v[9][i]); pb[i].y = pk2(v[10][i], v[11][i]); pb[i].z = pk2(v[12][i], v[13][i]); pb[i].w = pk2(v[14][i], v[15][i]); }
;         }
;         const int nit = it + NW; bf16_t* cdst = dst; const int cldd = ldd;
;         if (nit < hi) { cvt_resolve(P, nit, src, ldw, dst, ldd, qperm, f8);
; #pragma unroll
;             for (int rr = 0; rr < 16; ++rr) v[rr] = __builtin_nontemporal_load((const f32x4*)(src + (size_t)(16 * q + rr) * ldw + 4 * c)); }
;     ...
;         LDS_WAIT(); asm volatile("" ::: "memory");
;         if (nit >= hi) break;
;         it = nit;
	v_lshl_add_u64 v[2:3], s[8:9], 0, v[104:105]
	v_lshlrev_b64 v[4:5], s4, v[100:101]
	v_or_b32_e32 v108, 2, v100
	v_mov_b32_e32 v109, v105
	v_lshl_add_u64 v[4:5], v[4:5], 2, v[2:3]
	v_lshlrev_b64 v[6:7], s4, v[106:107]
	v_or_b32_e32 v110, 3, v100
	v_mov_b32_e32 v111, v105
	v_lshl_add_u64 v[6:7], v[6:7], 2, v[2:3]
	global_load_dwordx4 v[26:29], v[4:5], off nt
	global_load_dwordx4 v[30:33], v[6:7], off nt
	v_lshlrev_b64 v[4:5], s4, v[108:109]
	v_or_b32_e32 v112, 4, v100
	v_mov_b32_e32 v113, v105
	v_lshl_add_u64 v[4:5], v[4:5], 2, v[2:3]
	v_lshlrev_b64 v[6:7], s4, v[110:111]
	v_or_b32_e32 v114, 5, v100
	v_mov_b32_e32 v115, v105
	v_lshl_add_u64 v[6:7], v[6:7], 2, v[2:3]
	global_load_dwordx4 v[38:41], v[4:5], off nt
	global_load_dwordx4 v[42:45], v[6:7], off nt
	v_lshlrev_b64 v[4:5], s4, v[112:113]
	v_or_b32_e32 v116, 6, v100
	v_mov_b32_e32 v117, v105
	v_lshl_add_u64 v[4:5], v[4:5], 2, v[2:3]
	v_lshlrev_b64 v[6:7], s4, v[114:115]
	v_or_b32_e32 v118, 7, v100
	v_mov_b32_e32 v119, v105
	v_lshl_add_u64 v[6:7], v[6:7], 2, v[2:3]
	global_load_dwordx4 v[46:49], v[4:5], off nt
	global_load_dwordx4 v[50:53], v[6:7], off nt
	v_lshlrev_b64 v[4:5], s4, v[116:117]
	v_or_b32_e32 v120, 8, v100
	v_mov_b32_e32 v121, v105
	v_lshl_add_u64 v[4:5], v[4:5], 2, v[2:3]
	v_lshlrev_b64 v[6:7], s4, v[118:119]
	v_or_b32_e32 v122, 9, v100
	v_mov_b32_e32 v123, v105
	v_lshl_add_u64 v[6:7], v[6:7], 2, v[2:3]
	global_load_dwordx4 v[58:61], v[4:5], off nt
	global_load_dwordx4 v[62:65], v[6:7], off nt
	v_lshlrev_b64 v[4:5], s4, v[120:121]
	v_or_b32_e32 v124, 10, v100
	v_mov_b32_e32 v125, v105
	v_lshl_add_u64 v[4:5], v[4:5], 2, v[2:3]
	v_lshlrev_b64 v[6:7], s4, v[122:123]
	v_or_b32_e32 v126, 11, v100
	v_mov_b32_e32 v127, v105
	v_lshl_add_u64 v[6:7], v[6:7], 2, v[2:3]
	global_load_dwordx4 v[66:69], v[4:5], off nt
	global_load_dwordx4 v[70:73], v[6:7], off nt
	v_lshlrev_b64 v[4:5], s4, v[124:125]
	v_or_b32_e32 v128, 12, v100
	v_mov_b32_e32 v129, v105
	v_lshl_add_u64 v[4:5], v[4:5], 2, v[2:3]
	v_lshlrev_b64 v[6:7], s4, v[126:127]
	v_or_b32_e32 v130, 13, v100
	v_mov_b32_e32 v131, v105
	v_lshl_add_u64 v[6:7], v[6:7], 2, v[2:3]
	global_load_dwordx4 v[74:77], v[4:5], off nt
	global_load_dwordx4 v[78:81], v[6:7], off nt
	v_lshlrev_b64 v[4:5], s4, v[128:129]
	v_or_b32_e32 v132, 14, v100
	v_mov_b32_e32 v133, v105
	v_lshl_add_u64 v[4:5], v[4:5], 2, v[2:3]
	v_lshlrev_b64 v[6:7], s4, v[130:131]
	v_or_b32_e32 v134, 15, v194
	v_mov_b32_e32 v135, v105
	v_lshl_add_u64 v[6:7], v[6:7], 2, v[2:3]
	global_load_dwordx4 v[82:85], v[4:5], off nt
	global_load_dwordx4 v[86:89], v[6:7], off nt
	v_lshlrev_b64 v[4:5], s4, v[132:133]
	v_lshl_add_u64 v[4:5], v[4:5], 2, v[2:3]
	v_lshlrev_b64 v[6:7], s4, v[134:135]
	v_lshl_add_u64 v[2:3], v[6:7], 2, v[2:3]
	global_load_dwordx4 v[90:93], v[4:5], off nt
	global_load_dwordx4 v[94:97], v[2:3], off nt
	v_lshlrev_b32_e32 v2, 3, v0
	v_and_b32_e32 v3, 4, v137
	v_and_or_b32 v101, v2, 56, v3
	v_lshlrev_b32_e32 v2, 1, v0
	v_and_b32_e32 v2, 0x60, v2
	v_readlane_b32 s4, v250, 3
	v_readlane_b32 s11, v251, 25
	s_lshl_b32 s8, s2, 9
	v_add_u32_e32 v107, s4, v2
	v_and_b32_e32 v2, 7, v0
	s_lshl_b32 s10, s11, 6
	v_lshl_add_u32 v3, v2, 4, s4
	v_add_u32_e32 v109, s4, v100
	v_add_u32_e32 v4, s4, v98
	s_lshr_b32 s4, s69, 3
	s_add_i32 s8, s8, s10
	s_lshl_b32 s5, s4, 12
	s_add_i32 s30, s8, 0x1b0000
	s_lshl_b32 s8, s33, 9
	s_sub_i32 s29, 0, s5
	s_sub_i32 s31, s8, s5
	s_add_i32 s5, s11, s78
	s_lshl_b32 s10, s4, 7
	s_sub_i32 s34, s5, s10
	s_add_i32 s5, s86, s78
	s_sub_i32 s5, s5, s10
	s_lshl_b32 s5, s5, 3
	s_add_i32 s35, s5, 0x36000
	s_lshl_b32 s5, s33, 6
	s_lshl_b32 s10, s4, 9
	v_lshrrev_b32_e32 v136, 3, v194
	v_lshrrev_b32_e32 v152, 2, v194
	s_sub_i32 s36, s5, s10
	s_lshl_b32 s5, s4, 13
	s_lshl_b32 s4, s4, 6
	v_lshlrev_b32_e32 v2, 3, v2
	v_mul_u32_u24_e32 v5, 0x90, v136
	v_mul_u32_u24_e32 v6, 0x50, v152
	s_sub_i32 s4, s11, s4
	s_mov_b32 s9, 0
	v_mov_b32_e32 v99, v105
	v_or_b32_e32 v138, 8, v136
	v_or_b32_e32 v140, 16, v136
	v_or_b32_e32 v142, 24, v136
	v_or_b32_e32 v144, 32, v136
	v_or_b32_e32 v146, 40, v136
	v_or_b32_e32 v148, 48, v136
	v_or_b32_e32 v150, 56, v136
	v_or_b32_e32 v154, 16, v152
	v_or_b32_e32 v156, 32, v152
	v_or_b32_e32 v158, 48, v152
	s_sub_i32 s37, s8, s5
	s_add_i32 s38, s4, 0x6c00
	s_mov_b64 s[14:15], -1
	s_mov_b64 s[10:11], 0
	s_mov_b32 s39, 0xc3e00000
	v_lshlrev_b32_e32 v160, 1, v2
	v_add_u32_e32 v111, v3, v5
	v_add_u32_e32 v113, v4, v6
	v_mov_b32_e32 v115, 0x43e00000
	s_mov_b64 s[12:13], s[96:97]
	s_branch .LBB0_449
.LBB0_448:
	s_waitcnt lgkmcnt(0)
	s_add_i32 s38, s38, s26
	s_add_i32 s30, s30, s31
	s_add_i32 s34, s34, s26
	s_add_i32 s35, s35, s36
	s_add_i32 s0, s85, s38
	s_cmp_lt_i32 s0, 0xa080
	s_mov_b64 s[0:1], s[4:5]
	s_mov_b32 s28, s8
	s_mov_b64 s[10:11], s[18:19]
	s_mov_b64 s[14:15], s[16:17]
	s_cbranch_scc0 .LBB0_483

; DI void cvt_resolve(const CvtPtrs& P, int it, const float*& src, int& ldw, bf16_t*& dst, int& ldd, bool& qperm, bool& f8) {
;     int r = it; qperm = false; f8 = false;
;     if (r < 3072) { const int kt = ((r >> 3) / 96) * 8 + (r & 7), nt = (r >> 3) % 96, n0 = nt * 64, part = n0 >> 11, j0 = n0 & 2047;
;         src = P.cin + (size_t)(kt * 64) * 6144 + n0; ldw = 6144; ldd = DM;
;         dst = (part == 0 ? P.W1B + (size_t)j0 * DM : P.W1A + (size_t)((j0 >> 7) * 256 + (part == 2 ? 128 : 0) + (j0 & 127)) * DM) + kt * 64; return; } r -= 3072;
;     if (r < 1024) { const int kt = ((r >> 3) / 32) * 8 + (r & 7), nt = (r >> 3) % 32; src = P.cout + (size_t)(kt * 64) * DM + nt * 64; ldw = DM; dst = P.W2 + (size_t)(nt * 64) * DM + kt * 64; ldd = DM; return; } r -= 1024;
;     if (r < 1536) { const int kt = ((r >> 3) / 48) * 8 + (r & 7), nt = (r >> 3) % 48; src = P.wqkv + (size_t)(kt * 64) * 3072 + nt * 64; ldw = 3072; qperm = nt < 40;     f8 = true; dst = (bf16_t*)((unsigned char*)P.WQKV + (size_t)(nt * 64) * DM + kt * 64); ldd = DM;     return; } r -= 1536;
;     if (r < 1024) { const int kt = ((r >> 3) / 32) * 8 + (r & 7), nt = (r >> 3) % 32; src = P.wo + (size_t)(kt * 64) * DM + nt * 64; ldw = DM; f8 = true;
;         dst = (bf16_t*)((unsigned char*)P.WO + (size_t)(nt * 64) * DM + kt * 64); ldd = DM; return; } r -= 1024;
;     const int l = r / CVT_L, rr = r % CVT_L, kind = rr / 8192, q = rr % 8192, le = l * 16 + q / 512, rem = q % 512;
;     f8 = true;
;     if (kind < 2) { const int kt = ((rem >> 3) / 16) * 8 + (rem & 7), nt = (rem >> 3) % 16, n0 = nt * 64;
;         src = (kind ? P.wu : P.wg) + (size_t)le * DM * DFF + (size_t)(kt * 64) * DFF + n0; ldw = DFF;
;         dst = (bf16_t*)((unsigned char*)P.WGU + (size_t)(le * 2048 + (n0 >> 7) * 256 + kind * 128 + (n0 & 127)) * DM + kt * 64); ldd = DM; }
;     else { const int kt = ((rem >> 3) / 32) * 8 + (rem & 7), nt = (rem >> 3) % 32;
; DI void cvt_range(const CvtPtrs& P, int lo, int hi, int w, int NW, LAS unsigned* scr, int lane) {
;     ...
;         const int nit = it + NW; bf16_t* cdst = dst; const int cldd = ldd;
;         if (nit < hi) { cvt_resolve(P, nit, src, ldw, dst, ldd, qperm, f8);
; #pragma unroll
;             for (int rr = 0; rr < 16; ++rr) v[rr] = __builtin_nontemporal_load((const f32x4*)(src + (size_t)(16 * q + rr) * ldw + 4 * c)); }
.LBB0_453:
	s_add_i32 s57, s85, s34
	s_add_i32 s56, s57, 0x6c00
	s_cmp_gt_i32 s56, 0xa07f
	s_mov_b64 s[16:17], s[14:15]
	s_mov_b64 s[18:19], s[10:11]
	s_mov_b32 s8, s28
	s_mov_b64 s[4:5], s[0:1]
	s_cbranch_scc1 .LBB0_479
	s_cmpk_gt_i32 s56, 0xbff
	s_mov_b64 s[24:25], -1
	s_cbranch_scc0 .LBB0_472
	s_mov_b64 s[16:17], -1
	s_cmpk_gt_u32 s56, 0xfff
	s_cbranch_scc0 .LBB0_469
	s_cmpk_gt_u32 s56, 0x15ff
	s_mov_b64 s[18:19], -1
	s_cbranch_scc0 .LBB0_467
	s_cmpk_gt_u32 s56, 0x19ff
	s_cbranch_scc0 .LBB0_464
	s_add_i32 s4, s57, 0x5200
	s_add_i32 s5, s57, 0xfffff200
	s_cmpk_lt_u32 s4, 0x6000
	s_cselect_b32 s8, s4, s5
	s_cmpk_gt_u32 s4, 0x5fff
	s_cselect_b32 s4, 16, 0
	s_bfe_u32 s5, s8, 0x40009
	s_or_b32 s19, s5, s4
	s_and_b32 s20, s8, 7
	s_mov_b32 s25, s88
	s_cmpk_gt_u32 s8, 0x3fff
	s_mov_b64 s[4:5], -1
	s_cbranch_scc0 .LBB0_460
	s_lshr_b32 s4, s8, 5
	s_and_b32 s4, s4, 8
	v_readlane_b32 s44, v251, 28
	s_or_b32 s4, s4, s20
	s_lshl_b32 s5, s19, 23
	v_readlane_b32 s50, v251, 34
	v_readlane_b32 s51, v251, 35
	s_add_u32 s5, s50, s5
	s_addc_u32 s21, s51, 0
	s_lshl_b32 s18, s4, 6
	s_lshl_b32 s4, s4, 19
	s_add_u32 s4, s5, s4
	s_addc_u32 s5, s21, 0
	s_lshl_b32 s21, s8, 3
	s_and_b32 s21, s21, 0x7c0
	s_lshl_b32 s22, s21, 2
	s_add_u32 s22, s4, s22
	s_addc_u32 s23, s5, 0
	s_lshl_b32 s4, s19, 21
	s_lshl_b32 s5, s21, 10
	v_readlane_b32 s45, v251, 29
	v_readlane_b32 s46, v251, 30
	v_readlane_b32 s47, v251, 31
	v_readlane_b32 s48, v251, 32
	v_readlane_b32 s49, v251, 33
	s_or_b32 s24, s4, s5
	s_mov_b64 s[4:5], 0

; __device__ __forceinline__ unsigned cvt_pk_bf16(float lo, float hi) { unsigned r; asm volatile("v_cvt_pk_bf16_f32 %0, %1, %2" : "=v"(r) : "v"(lo), "v"(hi)); return r; }
; DI float bf_lo(unsigned w) { return __uint_as_float(w << 16); }
; DI float bf_hi(unsigned w) { return __uint_as_float(w & 0xffff0000u); }
; #define RES_LOAD(g_) do { const size_t off_ = RES_OFF(g_); _Pragma("unroll") for (int bj = 0; bj < 2; ++bj) { \
;             if (BASE_F32) { fb[(g_) % 3][bj][0] = *(const f32x4*)(base + off_ + bj * 128); fb[(g_) % 3][bj][1] = *(const f32x4*)(base + off_ + bj * 128 + 4); } \
;             else hb[(g_) % 3][bj] = *(const u32x4*)(out + off_ + bj * 128); } } while (0)
;     DI void operator()(const f32x4 (&acc)[2][2][4][2], const Unit& u, int wr, int wc, int fr, int fq) const {
;         const int rowt = u.pm * 256; const int cr = rowt < ML ? (rowt >> 11) : 8;
;         const float* base = rowt < ML ? base_lat : base_ctx - (size_t)ML * DM;
;         const int row0 = rowt + wr * 64 + fr, col0 = u.pn * 256 + wc * 32 + 8 * fq;
;         f32x4 gv[2][2];
; #pragma unroll
;         for (int bj = 0; bj < 2; ++bj)
; #pragma unroll
;             for (int n = 0; n < 2; ++n) gv[bj][n] = *(const f32x4*)(gate + (size_t)cr * NMOD + col0 + bj * 128 + n * 4) * ws;
;         f32x4 fb[BASE_F32 ? 3 : 1][2][2]; u32x4 hb[BASE_F32 ? 1 : 3][2];
;     ...
;         RES_LOAD(0); RES_LOAD(1); RES_LOAD(2);
; #pragma unroll
;         for (int g = 0; g < 8; ++g) { const int ai = g >> 2, m = g & 3; const size_t off = RES_OFF(g);
; #pragma unroll
;             for (int bj = 0; bj < 2; ++bj) { f32x4 b0, b1;
;                 if (BASE_F32) { b0 = fb[g % 3][bj][0]; b1 = fb[g % 3][bj][1]; }
;                 else { const u32x4 h4 = hb[g % 3][bj]; b0 = (f32x4){bf_lo(h4.x), bf_hi(h4.x), bf_lo(h4.y), bf_hi(h4.y)}; b1 = (f32x4){bf_lo(h4.z), bf_hi(h4.z), bf_lo(h4.w), bf_hi(h4.w)}; }
;                 const f32x4 v0 = b0 + gv[bj][0] * acc[ai][bj][m][0], v1 = b1 + gv[bj][1] * acc[ai][bj][m][1];
;                 u32x4 w; w.x = cvt_pk_bf16(v0[0], v0[1]); w.y = cvt_pk_bf16(v0[2], v0[3]); w.z = cvt_pk_bf16(v1[0], v1[1]); w.w = cvt_pk_bf16(v1[2], v1[3]);
;                 *(u32x4*)(out + off + bj * 128) = w; }
;             if (g + 3 < 8) RES_LOAD(g + 3);
;             __builtin_amdgcn_sched_barrier(0); }
.LBB0_497:
	v_readlane_b32 s40, v251, 9
	v_readlane_b32 s41, v251, 10
	v_readlane_b32 s42, v251, 11
	v_readlane_b32 s43, v251, 12
	v_readlane_b32 s44, v251, 13
	v_readlane_b32 s45, v251, 14
	v_readlane_b32 s46, v251, 15
	v_readlane_b32 s47, v251, 16
	v_readlane_b32 s48, v251, 17
	v_readlane_b32 s49, v251, 18
	v_readlane_b32 s50, v251, 19
	v_readlane_b32 s51, v251, 20
	v_readlane_b32 s52, v251, 21
	v_readlane_b32 s53, v251, 22
	v_readlane_b32 s54, v251, 23
	v_readlane_b32 s55, v251, 24
	s_min_i32 s4, s22, 64
	s_ashr_i32 s4, s4, 3
	s_mul_hi_i32 s5, s4, 0xc000
	s_mul_i32 s4, s4, 0xc000
	s_add_u32 s4, s57, s4
	s_addc_u32 s5, s58, s5
	v_lshl_or_b32 v244, s71, 8, v200
	v_lshl_add_u32 v249, s22, 8, v1
	v_lshlrev_b32_e32 v248, 13, v249
	v_lshl_add_u32 v248, v244, 2, v248
	v_lshlrev_b32_e32 v249, 12, v249
	v_lshl_add_u32 v249, v244, 1, v249
	v_lshlrev_b32_e32 v244, 2, v244
	global_load_dwordx4 v[122:125], v244, s[4:5]
	global_load_dwordx4 v[126:129], v244, s[4:5] offset:16
	global_load_dwordx4 v[190:193], v244, s[4:5] offset:512
	global_load_dwordx4 v[196:199], v244, s[4:5] offset:528
	s_cmp_lt_i32 s22, 64
	s_mov_b64 s[12:13], s[40:41]
	s_cselect_b32 s5, s13, s61
	s_cselect_b32 s4, s12, s60
	v_mov_b32_e32 v244, v248
	global_load_dwordx4 v[138:141], v244, s[4:5]
	global_load_dwordx4 v[142:145], v244, s[4:5] offset:16
	global_load_dwordx4 v[146:149], v244, s[4:5] offset:512
	global_load_dwordx4 v[150:153], v244, s[4:5] offset:528
	v_add_u32_e32 v244, 0x20000, v248
	global_load_dwordx4 v[154:157], v244, s[4:5]
	global_load_dwordx4 v[158:161], v244, s[4:5] offset:16
	global_load_dwordx4 v[162:165], v244, s[4:5] offset:512
	global_load_dwordx4 v[166:169], v244, s[4:5] offset:528
	v_add_u32_e32 v244, 0x40000, v248
	global_load_dwordx4 v[170:173], v244, s[4:5]
	global_load_dwordx4 v[174:177], v244, s[4:5] offset:16
	global_load_dwordx4 v[204:207], v244, s[4:5] offset:512
	global_load_dwordx4 v[208:211], v244, s[4:5] offset:528
	v_add_u32_e32 v244, 0x60000, v248
	global_load_dwordx4 v[212:215], v244, s[4:5]
	global_load_dwordx4 v[216:219], v244, s[4:5] offset:16
	global_load_dwordx4 v[220:223], v244, s[4:5] offset:512
	global_load_dwordx4 v[224:227], v244, s[4:5] offset:528
	v_add_u32_e32 v244, 0x100000, v248
	global_load_dwordx4 v[228:231], v244, s[4:5]
	global_load_dwordx4 v[232:235], v244, s[4:5] offset:16
	global_load_dwordx4 v[236:239], v244, s[4:5] offset:512
	global_load_dwordx4 v[240:243], v244, s[4:5] offset:528
	s_waitcnt vmcnt(16)
	v_mov_b32_e32 v244, v249
	v_pk_fma_f32 v[134:135], v[134:135], v[122:123], v[138:139]
	v_pk_fma_f32 v[136:137], v[136:137], v[124:125], v[140:141]
	v_pk_fma_f32 v[130:131], v[130:131], v[126:127], v[142:143]
	v_pk_fma_f32 v[132:133], v[132:133], v[128:129], v[144:145]
	v_pk_fma_f32 v[118:119], v[118:119], v[190:191], v[146:147]
	v_pk_fma_f32 v[120:121], v[120:121], v[192:193], v[148:149]
	v_pk_fma_f32 v[114:115], v[114:115], v[196:197], v[150:151]
	v_pk_fma_f32 v[116:117], v[116:117], v[198:199], v[152:153]
	v_cvt_pk_bf16_f32 v134, v134, v135
	v_cvt_pk_bf16_f32 v135, v136, v137
	v_cvt_pk_bf16_f32 v136, v130, v131
	v_cvt_pk_bf16_f32 v137, v132, v133
	global_store_dwordx4 v244, v[134:137], s[92:93]
	v_cvt_pk_bf16_f32 v118, v118, v119
	v_cvt_pk_bf16_f32 v119, v120, v121
	v_cvt_pk_bf16_f32 v120, v114, v115
	v_cvt_pk_bf16_f32 v121, v116, v117
	global_store_dwordx4 v244, v[118:121], s[92:93] offset:256
	s_nop 1
	v_add_u32_e32 v244, 0x120000, v248
	global_load_dwordx4 v[130:133], v244, s[4:5]
	global_load_dwordx4 v[114:117], v244, s[4:5] offset:16
	global_load_dwordx4 v[134:137], v244, s[4:5] offset:512
	global_load_dwordx4 v[118:121], v244, s[4:5] offset:528
	s_waitcnt vmcnt(18)
	v_add_u32_e32 v244, 0x10000, v249
	v_pk_fma_f32 v[110:111], v[110:111], v[122:123], v[154:155]
	v_pk_fma_f32 v[112:113], v[112:113], v[124:125], v[156:157]
	v_pk_fma_f32 v[106:107], v[106:107], v[126:127], v[158:159]
	v_pk_fma_f32 v[108:109], v[108:109], v[128:129], v[160:161]
	v_pk_fma_f32 v[102:103], v[102:103], v[190:191], v[162:163]
	v_pk_fma_f32 v[104:105], v[104:105], v[192:193], v[164:165]
	v_pk_fma_f32 v[98:99], v[98:99], v[196:197], v[166:167]
	v_pk_fma_f32 v[100:101], v[100:101], v[198:199], v[168:169]
	v_cvt_pk_bf16_f32 v110, v110, v111
	v_cvt_pk_bf16_f32 v111, v112, v113
	v_cvt_pk_bf16_f32 v112, v106, v107
	v_cvt_pk_bf16_f32 v113, v108, v109
	global_store_dwordx4 v244, v[110:113], s[92:93]
	v_cvt_pk_bf16_f32 v102, v102, v103
	v_cvt_pk_bf16_f32 v103, v104, v105
	v_cvt_pk_bf16_f32 v104, v98, v99
	v_cvt_pk_bf16_f32 v105, v100, v101
	global_store_dwordx4 v244, v[102:105], s[92:93] offset:256
	s_nop 1
	v_add_u32_e32 v244, 0x140000, v248
	global_load_dwordx4 v[106:109], v244, s[4:5]
	global_load_dwordx4 v[98:101], v244, s[4:5] offset:16
	global_load_dwordx4 v[110:113], v244, s[4:5] offset:512
	global_load_dwordx4 v[102:105], v244, s[4:5] offset:528
	s_waitcnt vmcnt(20)
; __device__ __forceinline__ unsigned cvt_pk_bf16(float lo, float hi) { unsigned r; asm volatile("v_cvt_pk_bf16_f32 %0, %1, %2" : "=v"(r) : "v"(lo), "v"(hi)); return r; }
; DI float bf_lo(unsigned w) { return __uint_as_float(w << 16); }
; DI float bf_hi(unsigned w) { return __uint_as_float(w & 0xffff0000u); }
; #define RES_LOAD(g_) do { const size_t off_ = RES_OFF(g_); _Pragma("unroll") for (int bj = 0; bj < 2; ++bj) { \
;             if (BASE_F32) { fb[(g_) % 3][bj][0] = *(const f32x4*)(base + off_ + bj * 128); fb[(g_) % 3][bj][1] = *(const f32x4*)(base + off_ + bj * 128 + 4); } \
;             else hb[(g_) % 3][bj] = *(const u32x4*)(out + off_ + bj * 128); } } while (0)
;     DI void operator()(const f32x4 (&acc)[2][2][4][2], const Unit& u, int wr, int wc, int fr, int fq) const {
;     ...
;         RES_LOAD(0); RES_LOAD(1); RES_LOAD(2);
; #pragma unroll
;         for (int g = 0; g < 8; ++g) { const int ai = g >> 2, m = g & 3; const size_t off = RES_OFF(g);
; #pragma unroll
;             for (int bj = 0; bj < 2; ++bj) { f32x4 b0, b1;
;                 if (BASE_F32) { b0 = fb[g % 3][bj][0]; b1 = fb[g % 3][bj][1]; }
;                 else { const u32x4 h4 = hb[g % 3][bj]; b0 = (f32x4){bf_lo(h4.x), bf_hi(h4.x), bf_lo(h4.y), bf_hi(h4.y)}; b1 = (f32x4){bf_lo(h4.z), bf_hi(h4.z), bf_lo(h4.w), bf_hi(h4.w)}; }
;                 const f32x4 v0 = b0 + gv[bj][0] * acc[ai][bj][m][0], v1 = b1 + gv[bj][1] * acc[ai][bj][m][1];
;                 u32x4 w; w.x = cvt_pk_bf16(v0[0], v0[1]); w.y = cvt_pk_bf16(v0[2], v0[3]); w.z = cvt_pk_bf16(v1[0], v1[1]); w.w = cvt_pk_bf16(v1[2], v1[3]);
;                 *(u32x4*)(out + off + bj * 128) = w; }
;             if (g + 3 < 8) RES_LOAD(g + 3);
;             __builtin_amdgcn_sched_barrier(0); }
	v_add_u32_e32 v244, 0x20000, v249
	v_pk_fma_f32 v[94:95], v[94:95], v[122:123], v[170:171]
	v_pk_fma_f32 v[96:97], v[96:97], v[124:125], v[172:173]
	v_pk_fma_f32 v[90:91], v[90:91], v[126:127], v[174:175]
	v_pk_fma_f32 v[92:93], v[92:93], v[128:129], v[176:177]
	v_pk_fma_f32 v[86:87], v[86:87], v[190:191], v[204:205]
	v_pk_fma_f32 v[88:89], v[88:89], v[192:193], v[206:207]
	v_pk_fma_f32 v[82:83], v[82:83], v[196:197], v[208:209]
	v_pk_fma_f32 v[84:85], v[84:85], v[198:199], v[210:211]
	v_cvt_pk_bf16_f32 v94, v94, v95
	v_cvt_pk_bf16_f32 v95, v96, v97
	v_cvt_pk_bf16_f32 v96, v90, v91
	v_cvt_pk_bf16_f32 v97, v92, v93
	global_store_dwordx4 v244, v[94:97], s[92:93]
	v_cvt_pk_bf16_f32 v86, v86, v87
	v_cvt_pk_bf16_f32 v87, v88, v89
	v_cvt_pk_bf16_f32 v88, v82, v83
	v_cvt_pk_bf16_f32 v89, v84, v85
	global_store_dwordx4 v244, v[86:89], s[92:93] offset:256
	s_nop 1
	v_add_u32_e32 v244, 0x160000, v248
	global_load_dwordx4 v[90:93], v244, s[4:5]
	global_load_dwordx4 v[82:85], v244, s[4:5] offset:16
	global_load_dwordx4 v[94:97], v244, s[4:5] offset:512
	global_load_dwordx4 v[86:89], v244, s[4:5] offset:528
	s_waitcnt vmcnt(22)
	v_add_u32_e32 v244, 0x30000, v249
	v_pk_fma_f32 v[78:79], v[78:79], v[122:123], v[212:213]
	v_pk_fma_f32 v[80:81], v[80:81], v[124:125], v[214:215]
	v_pk_fma_f32 v[74:75], v[74:75], v[126:127], v[216:217]
	v_pk_fma_f32 v[76:77], v[76:77], v[128:129], v[218:219]
	v_pk_fma_f32 v[70:71], v[70:71], v[190:191], v[220:221]
	v_pk_fma_f32 v[72:73], v[72:73], v[192:193], v[222:223]
	v_pk_fma_f32 v[66:67], v[66:67], v[196:197], v[224:225]
	v_pk_fma_f32 v[68:69], v[68:69], v[198:199], v[226:227]
	v_cvt_pk_bf16_f32 v78, v78, v79
	v_cvt_pk_bf16_f32 v79, v80, v81
	v_cvt_pk_bf16_f32 v80, v74, v75
	v_cvt_pk_bf16_f32 v81, v76, v77
	global_store_dwordx4 v244, v[78:81], s[92:93]
	v_cvt_pk_bf16_f32 v70, v70, v71
	v_cvt_pk_bf16_f32 v71, v72, v73
	v_cvt_pk_bf16_f32 v72, v66, v67
	v_cvt_pk_bf16_f32 v73, v68, v69
	global_store_dwordx4 v244, v[70:73], s[92:93] offset:256
	s_waitcnt vmcnt(20)
	v_add_u32_e32 v244, 0x80000, v249
	v_pk_fma_f32 v[62:63], v[62:63], v[122:123], v[228:229]
	v_pk_fma_f32 v[64:65], v[64:65], v[124:125], v[230:231]
	v_pk_fma_f32 v[58:59], v[58:59], v[126:127], v[232:233]
	v_pk_fma_f32 v[60:61], v[60:61], v[128:129], v[234:235]
	v_pk_fma_f32 v[54:55], v[54:55], v[190:191], v[236:237]
	v_pk_fma_f32 v[56:57], v[56:57], v[192:193], v[238:239]
	v_pk_fma_f32 v[50:51], v[50:51], v[196:197], v[240:241]
	v_pk_fma_f32 v[52:53], v[52:53], v[198:199], v[242:243]
	v_cvt_pk_bf16_f32 v62, v62, v63
	v_cvt_pk_bf16_f32 v63, v64, v65
	v_cvt_pk_bf16_f32 v64, v58, v59
	v_cvt_pk_bf16_f32 v65, v60, v61
	global_store_dwordx4 v244, v[62:65], s[92:93]
	v_cvt_pk_bf16_f32 v54, v54, v55
	v_cvt_pk_bf16_f32 v55, v56, v57
	v_cvt_pk_bf16_f32 v56, v50, v51
	v_cvt_pk_bf16_f32 v57, v52, v53
	global_store_dwordx4 v244, v[54:57], s[92:93] offset:256
	s_waitcnt vmcnt(16)
	v_add_u32_e32 v244, 0x90000, v249
	v_pk_fma_f32 v[46:47], v[46:47], v[122:123], v[130:131]
	v_pk_fma_f32 v[48:49], v[48:49], v[124:125], v[132:133]
	v_pk_fma_f32 v[42:43], v[42:43], v[126:127], v[114:115]
	v_pk_fma_f32 v[44:45], v[44:45], v[128:129], v[116:117]
	v_pk_fma_f32 v[38:39], v[38:39], v[190:191], v[134:135]
	v_pk_fma_f32 v[40:41], v[40:41], v[192:193], v[136:137]
	v_pk_fma_f32 v[30:31], v[30:31], v[196:197], v[118:119]
	v_pk_fma_f32 v[32:33], v[32:33], v[198:199], v[120:121]
	v_cvt_pk_bf16_f32 v46, v46, v47
	v_cvt_pk_bf16_f32 v47, v48, v49
	v_cvt_pk_bf16_f32 v48, v42, v43
	v_cvt_pk_bf16_f32 v49, v44, v45
	global_store_dwordx4 v244, v[46:49], s[92:93]
	v_cvt_pk_bf16_f32 v38, v38, v39
	v_cvt_pk_bf16_f32 v39, v40, v41
	v_cvt_pk_bf16_f32 v40, v30, v31
	v_cvt_pk_bf16_f32 v41, v32, v33
	global_store_dwordx4 v244, v[38:41], s[92:93] offset:256
	s_waitcnt vmcnt(12)
	v_add_u32_e32 v244, 0xa0000, v249
	v_pk_fma_f32 v[34:35], v[34:35], v[122:123], v[106:107]
	v_pk_fma_f32 v[36:37], v[36:37], v[124:125], v[108:109]
	v_pk_fma_f32 v[26:27], v[26:27], v[126:127], v[98:99]
	v_pk_fma_f32 v[28:29], v[28:29], v[128:129], v[100:101]
	v_pk_fma_f32 v[22:23], v[22:23], v[190:191], v[110:111]
	v_pk_fma_f32 v[24:25], v[24:25], v[192:193], v[112:113]
	v_pk_fma_f32 v[14:15], v[14:15], v[196:197], v[102:103]
	v_pk_fma_f32 v[16:17], v[16:17], v[198:199], v[104:105]
	v_cvt_pk_bf16_f32 v34, v34, v35
	v_cvt_pk_bf16_f32 v35, v36, v37
	v_cvt_pk_bf16_f32 v36, v26, v27
	v_cvt_pk_bf16_f32 v37, v28, v29
	global_store_dwordx4 v244, v[34:37], s[92:93]
	v_cvt_pk_bf16_f32 v22, v22, v23
	v_cvt_pk_bf16_f32 v23, v24, v25
	v_cvt_pk_bf16_f32 v24, v14, v15
	v_cvt_pk_bf16_f32 v25, v16, v17
	global_store_dwordx4 v244, v[22:25], s[92:93] offset:256
	s_waitcnt vmcnt(8)
	v_add_u32_e32 v244, 0xb0000, v249
	v_pk_fma_f32 v[18:19], v[18:19], v[122:123], v[90:91]
	v_pk_fma_f32 v[20:21], v[20:21], v[124:125], v[92:93]
	v_pk_fma_f32 v[10:11], v[10:11], v[126:127], v[82:83]
	v_pk_fma_f32 v[12:13], v[12:13], v[128:129], v[84:85]
	v_pk_fma_f32 v[6:7], v[6:7], v[190:191], v[94:95]
	v_pk_fma_f32 v[8:9], v[8:9], v[192:193], v[96:97]
	v_pk_fma_f32 v[2:3], v[2:3], v[196:197], v[86:87]
	v_pk_fma_f32 v[4:5], v[4:5], v[198:199], v[88:89]
	v_cvt_pk_bf16_f32 v18, v18, v19
	v_cvt_pk_bf16_f32 v19, v20, v21
	v_cvt_pk_bf16_f32 v20, v10, v11
	v_cvt_pk_bf16_f32 v21, v12, v13
	global_store_dwordx4 v244, v[18:21], s[92:93]
	v_cvt_pk_bf16_f32 v6, v6, v7
	v_cvt_pk_bf16_f32 v7, v8, v9
	v_cvt_pk_bf16_f32 v8, v2, v3
	v_cvt_pk_bf16_f32 v9, v4, v5
	global_store_dwordx4 v244, v[6:9], s[92:93] offset:256
	s_andn2_b64 vcc, exec, s[0:1]
	s_mov_b64 s[0:1], -1
	v_readlane_b32 s78, v250, 12
	v_readlane_b32 s79, v250, 13
	s_cbranch_vccnz .LBB0_490
	s_andn2_b64 vcc, exec, s[8:9]
	s_cbranch_vccnz .LBB0_489
	s_barrier
	s_branch .LBB0_489

; #define LAS __attribute__((address_space(3)))
; DI void cvt_resolve(const CvtPtrs& P, int it, const float*& src, int& ldw, bf16_t*& dst, int& ldd, bool& qperm, bool& f8) {
;     ...
;     const int l = r / CVT_L, rr = r % CVT_L, kind = rr / 8192, q = rr % 8192, le = l * 16 + q / 512, rem = q % 512;
;     f8 = true;
;     if (kind < 2) { const int kt = ((rem >> 3) / 16) * 8 + (rem & 7), nt = (rem >> 3) % 16, n0 = nt * 64;
;         src = (kind ? P.wu : P.wg) + (size_t)le * DM * DFF + (size_t)(kt * 64) * DFF + n0; ldw = DFF;
;         dst = (bf16_t*)((unsigned char*)P.WGU + (size_t)(le * 2048 + (n0 >> 7) * 256 + kind * 128 + (n0 & 127)) * DM + kt * 64); ldd = DM; }
;     else { const int kt = ((rem >> 3) / 32) * 8 + (rem & 7), nt = (rem >> 3) % 32;
;         src = P.wd + (size_t)le * DFF * DM + (size_t)(kt * 64) * DM + nt * 64; ldw = DM; dst = (bf16_t*)((unsigned char*)P.WDN + (size_t)(le * 2048 + nt * 64) * DFF + kt * 64); ldd = DFF; }
; }
; DI void cvt_range(const CvtPtrs& P, int lo, int hi, int w, int NW, LAS unsigned* scr, int lane) {
;     int it = lo + w; if (it >= hi) return;
;     const int c = lane & 15, q = lane >> 4;
;     const float* src; int ldw; bf16_t* dst; int ldd; bool qperm, f8; cvt_resolve(P, it, src, ldw, dst, ldd, qperm, f8);
;     f32x4 v[16];
; #pragma unroll
;     for (int rr = 0; rr < 16; ++rr) v[rr] = __builtin_nontemporal_load((const f32x4*)(src + (size_t)(16 * q + rr) * ldw + 4 * c));
.LBB0_850:
	s_abs_i32 s5, s33
	v_cvt_f32_u32_e32 v2, s5
	s_add_i32 s4, s33, 0x47f
	s_xor_b32 s6, s4, s33
	s_abs_i32 s7, s4
	v_rcp_iflag_f32_e32 v2, v2
	s_sub_i32 s8, 0, s5
	s_ashr_i32 s4, s6, 31
	v_mul_f32_e32 v2, 0x4f7ffffe, v2
	v_cvt_u32_f32_e32 v2, v2
	s_nop 0
	v_readfirstlane_b32 s6, v2
	s_mul_i32 s8, s8, s6
	s_mul_hi_u32 s8, s6, s8
	s_add_i32 s6, s6, s8
	s_mul_hi_u32 s6, s7, s6
	s_mul_i32 s8, s6, s5
	s_sub_i32 s7, s7, s8
	s_add_i32 s9, s6, 1
	s_sub_i32 s8, s7, s5
	s_cmp_ge_u32 s7, s5
	s_cselect_b32 s6, s9, s6
	s_cselect_b32 s7, s8, s7
	s_add_i32 s8, s6, 1
	s_cmp_ge_u32 s7, s5
	s_cselect_b32 s5, s8, s6
	s_xor_b32 s8, s5, s4
	s_sub_i32 s9, s8, s4
	s_add_i32 s10, s9, -1
	s_mul_i32 s10, s10, s33
	s_sub_i32 s6, 0x480, s10
	s_cmp_lt_i32 s2, s6
	s_cbranch_scc1 .LBB0_888
	s_sub_i32 s5, s2, s6
	s_lshl_b32 s5, s5, 3
	v_readlane_b32 s7, v251, 25
	s_add_i32 s5, s5, s7
	s_cmpk_gt_u32 s5, 0xfbf
	s_cbranch_scc1 .LBB0_888
	s_add_i32 s11, s5, 0x2680
	s_lshr_b32 s5, s11, 4
	v_readlane_b32 s16, v251, 28
	s_sub_i32 s6, s33, s6
	s_bfe_u32 s25, s88, 0x30006
	s_lshr_b32 s12, s11, 9
	s_and_b32 s5, s5, 24
	v_readlane_b32 s17, v251, 29
	v_readlane_b32 s18, v251, 30
	v_readlane_b32 s19, v251, 31
	v_readlane_b32 s20, v251, 32
	v_readlane_b32 s21, v251, 33
	s_lshl_b32 s24, s6, 3
	s_or_b32 s5, s5, s25
	s_lshl_b32 s13, s11, 3
	s_lshl_b32 s6, s12, 23
	v_readlane_b32 s22, v251, 34
	v_readlane_b32 s23, v251, 35
	s_mov_b64 s[16:17], s[20:21]
	s_add_u32 s6, s16, s6
	s_addc_u32 s7, s17, 0
	s_lshl_b32 s14, s5, 6
	s_lshl_b32 s5, s5, 18
	s_add_u32 s5, s6, s5
	s_addc_u32 s7, s7, 0
	s_lshl_b32 s6, s11, 5
	s_and_b32 s6, s6, 0xf00
	v_and_b32_e32 v98, 48, v0
	v_and_b32_e32 v100, 60, v195
	v_mov_b32_e32 v103, 0
	s_add_u32 s6, s5, s6
	v_or_b32_e32 v104, 1, v98
	s_addc_u32 s7, s7, 0
	v_lshlrev_b32_e32 v26, 2, v100
	v_mov_b32_e32 v27, v103
	v_lshlrev_b32_e32 v102, 12, v98
	v_lshlrev_b32_e32 v2, 12, v104
	s_waitcnt lgkmcnt(0)
	v_mov_b32_e32 v3, v103
	v_or_b32_e32 v106, 2, v98
	v_lshl_add_u64 v[48:49], s[6:7], 0, v[26:27]
	v_lshlrev_b32_e32 v4, 12, v106
	v_mov_b32_e32 v5, v103
	v_or_b32_e32 v108, 3, v98
	v_or_b32_e32 v110, 4, v98
	v_lshl_add_u64 v[26:27], v[48:49], 0, v[102:103]
	v_lshl_add_u64 v[2:3], v[48:49], 0, v[2:3]
	v_lshlrev_b32_e32 v6, 12, v108
	v_mov_b32_e32 v7, v103
	v_lshlrev_b32_e32 v8, 12, v110
	v_mov_b32_e32 v9, v103
	v_or_b32_e32 v112, 5, v98
	v_or_b32_e32 v114, 6, v98
	global_load_dwordx4 v[26:29], v[26:27], off nt
	s_nop 0
	global_load_dwordx4 v[30:33], v[2:3], off nt
	v_lshl_add_u64 v[2:3], v[48:49], 0, v[4:5]
	v_lshlrev_b32_e32 v10, 12, v112
	v_mov_b32_e32 v11, v103
	v_lshlrev_b32_e32 v12, 12, v114
	v_mov_b32_e32 v13, v103
	v_or_b32_e32 v116, 7, v98
	v_or_b32_e32 v118, 8, v98
	v_lshl_add_u64 v[4:5], v[48:49], 0, v[6:7]
	global_load_dwordx4 v[38:41], v[2:3], off nt
	global_load_dwordx4 v[42:45], v[4:5], off nt
	v_lshl_add_u64 v[2:3], v[48:49], 0, v[8:9]
	v_lshlrev_b32_e32 v14, 12, v116
	v_mov_b32_e32 v15, v103
	v_lshlrev_b32_e32 v16, 12, v118
	v_mov_b32_e32 v17, v103
	v_or_b32_e32 v120, 9, v98
	v_or_b32_e32 v122, 10, v98
	v_lshl_add_u64 v[4:5], v[48:49], 0, v[10:11]
	global_load_dwordx4 v[50:53], v[2:3], off nt
	global_load_dwordx4 v[54:57], v[4:5], off nt
	v_lshl_add_u64 v[2:3], v[48:49], 0, v[12:13]
	v_lshlrev_b32_e32 v18, 12, v120
	v_mov_b32_e32 v19, v103
	v_lshlrev_b32_e32 v20, 12, v122
	v_mov_b32_e32 v21, v103
	v_or_b32_e32 v124, 11, v98
	v_or_b32_e32 v126, 12, v98
	v_lshl_add_u64 v[4:5], v[48:49], 0, v[14:15]
	global_load_dwordx4 v[58:61], v[2:3], off nt
	global_load_dwordx4 v[62:65], v[4:5], off nt
	v_lshl_add_u64 v[2:3], v[48:49], 0, v[16:17]
	v_lshlrev_b32_e32 v22, 12, v124
	v_mov_b32_e32 v23, v103
	v_lshlrev_b32_e32 v24, 12, v126
	v_mov_b32_e32 v25, v103
	v_or_b32_e32 v128, 13, v98
	v_or_b32_e32 v130, 14, v98
	v_lshl_add_u64 v[4:5], v[48:49], 0, v[18:19]
	global_load_dwordx4 v[66:69], v[2:3], off nt
	global_load_dwordx4 v[70:73], v[4:5], off nt
	v_lshl_add_u64 v[2:3], v[48:49], 0, v[20:21]
	v_lshlrev_b32_e32 v34, 12, v128
	v_mov_b32_e32 v35, v103
	v_lshlrev_b32_e32 v36, 12, v130
	v_mov_b32_e32 v37, v103
	v_or_b32_e32 v132, 15, v194
	v_lshl_add_u64 v[4:5], v[48:49], 0, v[22:23]
	global_load_dwordx4 v[74:77], v[2:3], off nt
	global_load_dwordx4 v[78:81], v[4:5], off nt
	v_lshl_add_u64 v[2:3], v[48:49], 0, v[24:25]
	v_lshlrev_b32_e32 v46, 12, v132
	v_mov_b32_e32 v47, v103
	v_lshl_add_u64 v[4:5], v[48:49], 0, v[34:35]
	global_load_dwordx4 v[82:85], v[2:3], off nt
	global_load_dwordx4 v[86:89], v[4:5], off nt
	v_lshl_add_u64 v[2:3], v[48:49], 0, v[36:37]
	v_lshl_add_u64 v[4:5], v[48:49], 0, v[46:47]
	global_load_dwordx4 v[90:93], v[2:3], off nt
	global_load_dwordx4 v[94:97], v[4:5], off nt
	v_lshlrev_b32_e32 v2, 3, v0
	v_and_b32_e32 v1, 4, v1
	v_and_or_b32 v1, v2, 56, v1
	v_lshlrev_b32_e32 v2, 1, v0
	v_and_b32_e32 v2, 0x60, v2
	v_readlane_b32 s6, v250, 3
	s_lshl_b32 s7, s11, 4
	s_and_b32 s7, s7, 0x700
	v_add_u32_e32 v99, s6, v2
	v_and_b32_e32 v2, 7, v0
	v_lshl_add_u32 v3, v2, 4, s6
	v_add_u32_e32 v101, s6, v98
	v_add_u32_e32 v4, s6, v196
	s_lshl_b32 s6, s12, 11
	s_or_b32 s6, s6, s7
	s_and_b32 s7, s13, 64
	s_or_b32 s6, s6, s7
	s_lshl_b32 s6, s6, 11
	v_readlane_b32 s7, v250, 7
	s_add_u32 s6, s7, s6
	v_readlane_b32 s7, v250, 8
	s_addc_u32 s7, s7, 0
	s_add_u32 s6, s6, s14
	s_addc_u32 s7, s7, 0
	s_add_u32 s6, s6, 0x40000
	v_readlane_b32 s12, v251, 25
	s_addc_u32 s7, s7, 0
	s_lshl_b32 s26, s10, 9
	s_lshl_b32 s10, s2, 9
	s_lshl_b32 s11, s12, 6
	s_add_i32 s27, s10, s11
	s_lshl_b32 s10, s8, 4
	s_lshl_b32 s11, s4, 4
	s_sub_i32 s10, s10, s11
	s_add_i32 s10, s10, -8
	s_lshl_b32 s8, s8, 3
	s_lshl_b32 s4, s4, 3
	s_mul_i32 s10, s33, s10
	s_sub_i32 s4, s8, s4
	s_add_i32 s29, s12, s10
	s_add_i32 s4, s4, -8
	v_lshrrev_b32_e32 v134, 3, v194
	v_lshrrev_b32_e32 v150, 2, v194
	s_mul_i32 s9, s33, s9
	s_add_i32 s11, s29, s85
	s_mul_i32 s4, s33, s4
	v_lshlrev_b32_e32 v2, 3, v2
	v_mul_u32_u24_e32 v5, 0x90, v134
	v_mul_u32_u24_e32 v6, 0x50, v150
	s_lshl_b32 s28, s9, 9
	s_lshl_b32 s11, s11, 3
	s_lshl_b32 s31, s9, 6
	s_lshl_b32 s34, s10, 6
	s_add_i32 s4, s12, s4
	s_mov_b32 s5, 0
	v_mov_b32_e32 v197, v103
	v_or_b32_e32 v136, 8, v134
	v_or_b32_e32 v138, 16, v134
	v_or_b32_e32 v140, 24, v134
	v_or_b32_e32 v142, 32, v134
	v_or_b32_e32 v144, 40, v134
	v_or_b32_e32 v146, 48, v134
	v_or_b32_e32 v148, 56, v134
	v_or_b32_e32 v152, 16, v150
	v_or_b32_e32 v154, 32, v150
	v_or_b32_e32 v156, 48, v150
	s_add_i32 s26, s26, 0x1f2000
	s_add_i32 s28, s28, 0xfff70000
	s_add_i32 s30, s11, 0x2c400
	s_add_i32 s31, s31, 0xfffee000
	s_add_i32 s34, s34, 0x162000
	s_add_i32 s35, s4, 0x7c80
	s_mov_b64 s[10:11], -1
	s_mov_b64 s[8:9], 0
	s_movk_i32 s37, 0x800
	s_mov_b32 s36, 0xc3e00000
	v_lshlrev_b32_e32 v158, 1, v2
	v_add_u32_e32 v105, v3, v5
	v_add_u32_e32 v107, v4, v6
	v_mov_b32_e32 v109, 0x43e00000
	s_mov_b64 s[18:19], s[22:23]
	s_branch .LBB0_854
; #define LAS __attribute__((address_space(3)))
; #define LDS_WAIT() asm volatile("s_waitcnt lgkmcnt(0)" ::: "memory")
; DI void cvt_range(const CvtPtrs& P, int lo, int hi, int w, int NW, LAS unsigned* scr, int lane) {
;     ...
;         const int nit = it + NW; bf16_t* cdst = dst; const int cldd = ldd;
;         if (nit < hi) { cvt_resolve(P, nit, src, ldw, dst, ldd, qperm, f8);
; #pragma unroll
;             for (int rr = 0; rr < 16; ++rr) v[rr] = __builtin_nontemporal_load((const f32x4*)(src + (size_t)(16 * q + rr) * ldw + 4 * c)); }
;         if (cf8) {
; #pragma unroll
;             for (int i = 0; i < 4; ++i) *(LAS u32x4*)(scr + (wrow + i) * 20 + 4 * q) = pa[i];
;             LDS_WAIT(); asm volatile("" ::: "memory");
; #pragma unroll
;             for (int j = 0; j < 4; ++j) { const int ch = lane + 64 * j, n = ch >> 2, part = ch & 3; const u32x4 o = *(const LAS u32x4*)(scr + n * 20 + 4 * part);
;                 *(u32x4*)((unsigned char*)cdst + (size_t)n * cldd + 16 * part) = o; }
;         } else {
; #pragma unroll
;             for (int i = 0; i < 4; ++i) { *(LAS u32x4*)(scr + (wrow + i) * CVT_P + 8 * q) = pa[i]; *(LAS u32x4*)(scr + (wrow + i) * CVT_P + 8 * q + 4) = pb[i]; }
;             LDS_WAIT(); asm volatile("" ::: "memory");
; #pragma unroll
;             for (int j = 0; j < 8; ++j) { const int n = (lane >> 3) + 8 * j; const u32x4 o = *(const LAS u32x4*)(scr + n * CVT_P + 4 * (lane & 7));
;                 *(u32x4*)(cdst + (size_t)n * cldd + 8 * (lane & 7)) = o; }
;         }
;         LDS_WAIT(); asm volatile("" ::: "memory");
;         if (nit >= hi) break;
;         it = nit;
.LBB0_853:
	s_waitcnt lgkmcnt(0)
	s_add_i32 s35, s35, s24
	s_add_i32 s27, s27, s28
	s_add_i32 s29, s29, s24
	s_add_i32 s30, s30, s31
	s_add_i32 s6, s85, s35
	s_cmp_lt_i32 s6, 0xb040
	s_mov_b64 s[6:7], s[14:15]
	s_mov_b32 s37, s4
	s_mov_b64 s[8:9], s[16:17]
	s_mov_b64 s[10:11], s[12:13]
	s_cbranch_scc0 .LBB0_888

; DI void cvt_resolve(const CvtPtrs& P, int it, const float*& src, int& ldw, bf16_t*& dst, int& ldd, bool& qperm, bool& f8) {
;     int r = it; qperm = false; f8 = false;
;     if (r < 3072) { const int kt = ((r >> 3) / 96) * 8 + (r & 7), nt = (r >> 3) % 96, n0 = nt * 64, part = n0 >> 11, j0 = n0 & 2047;
;         src = P.cin + (size_t)(kt * 64) * 6144 + n0; ldw = 6144; ldd = DM;
;         dst = (part == 0 ? P.W1B + (size_t)j0 * DM : P.W1A + (size_t)((j0 >> 7) * 256 + (part == 2 ? 128 : 0) + (j0 & 127)) * DM) + kt * 64; return; } r -= 3072;
;     if (r < 1024) { const int kt = ((r >> 3) / 32) * 8 + (r & 7), nt = (r >> 3) % 32; src = P.cout + (size_t)(kt * 64) * DM + nt * 64; ldw = DM; dst = P.W2 + (size_t)(nt * 64) * DM + kt * 64; ldd = DM; return; } r -= 1024;
;     if (r < 1536) { const int kt = ((r >> 3) / 48) * 8 + (r & 7), nt = (r >> 3) % 48; src = P.wqkv + (size_t)(kt * 64) * 3072 + nt * 64; ldw = 3072; qperm = nt < 40;     f8 = true; dst = (bf16_t*)((unsigned char*)P.WQKV + (size_t)(nt * 64) * DM + kt * 64); ldd = DM;     return; } r -= 1536;
;     if (r < 1024) { const int kt = ((r >> 3) / 32) * 8 + (r & 7), nt = (r >> 3) % 32; src = P.wo + (size_t)(kt * 64) * DM + nt * 64; ldw = DM; f8 = true;
;         dst = (bf16_t*)((unsigned char*)P.WO + (size_t)(nt * 64) * DM + kt * 64); ldd = DM; return; } r -= 1024;
;     const int l = r / CVT_L, rr = r % CVT_L, kind = rr / 8192, q = rr % 8192, le = l * 16 + q / 512, rem = q % 512;
;     f8 = true;
;     if (kind < 2) { const int kt = ((rem >> 3) / 16) * 8 + (rem & 7), nt = (rem >> 3) % 16, n0 = nt * 64;
;         src = (kind ? P.wu : P.wg) + (size_t)le * DM * DFF + (size_t)(kt * 64) * DFF + n0; ldw = DFF;
;         dst = (bf16_t*)((unsigned char*)P.WGU + (size_t)(le * 2048 + (n0 >> 7) * 256 + kind * 128 + (n0 & 127)) * DM + kt * 64); ldd = DM; }
;     else { const int kt = ((rem >> 3) / 32) * 8 + (rem & 7), nt = (rem >> 3) % 32;
;         src = P.wd + (size_t)le * DFF * DM + (size_t)(kt * 64) * DM + nt * 64; ldw = DM; dst = (bf16_t*)((unsigned char*)P.WDN + (size_t)(le * 2048 + nt * 64) * DFF + kt * 64); ldd = DFF; }
; }
.LBB0_858:
	s_add_i32 s39, s85, s29
	s_add_i32 s38, s39, 0x5880
	s_cmp_gt_i32 s38, 0xb03f
	s_mov_b64 s[12:13], s[10:11]
	s_mov_b64 s[16:17], s[8:9]
	s_mov_b32 s4, s37
	s_mov_b64 s[14:15], s[6:7]
	s_cbranch_scc1 .LBB0_884
	s_cmpk_gt_i32 s38, 0xbff
	s_mov_b64 s[22:23], -1
	s_cbranch_scc0 .LBB0_877
	s_mov_b64 s[12:13], -1
	s_cmpk_gt_u32 s38, 0xfff
	s_cbranch_scc0 .LBB0_874
	s_cmpk_gt_u32 s38, 0x15ff
	s_mov_b64 s[16:17], -1
	s_cbranch_scc0 .LBB0_872
	s_cmpk_gt_u32 s38, 0x19ff
	s_cbranch_scc0 .LBB0_869
	s_add_i32 s14, s39, 0x3e80
	s_add_i32 s4, s39, 0xffffde80
	s_cmpk_lt_u32 s14, 0x6000
	s_cselect_b32 s4, s14, s4
	s_cmpk_gt_u32 s14, 0x5fff
	s_cselect_b32 s14, 16, 0
	s_bfe_u32 s15, s4, 0x40009
	s_or_b32 s17, s15, s14
	s_and_b32 s18, s4, 7
	s_mov_b32 s40, s88
	s_cmpk_gt_u32 s4, 0x3fff
	s_mov_b64 s[14:15], -1
	s_cbranch_scc0 .LBB0_865
	s_lshr_b32 s14, s4, 5
	s_and_b32 s14, s14, 8
	v_readlane_b32 s44, v251, 28
	s_or_b32 s14, s14, s18
	s_lshl_b32 s15, s17, 23
	v_readlane_b32 s50, v251, 34
	v_readlane_b32 s51, v251, 35
	s_add_u32 s15, s50, s15
	s_addc_u32 s19, s51, 0
	s_lshl_b32 s16, s14, 6
	s_lshl_b32 s14, s14, 19
	s_add_u32 s14, s15, s14
	s_addc_u32 s15, s19, 0
	s_lshl_b32 s19, s4, 3
	s_and_b32 s19, s19, 0x7c0
	s_lshl_b32 s20, s19, 2
	s_add_u32 s20, s14, s20
	s_addc_u32 s21, s15, 0
	s_lshl_b32 s14, s17, 21
	s_lshl_b32 s15, s19, 10
	v_readlane_b32 s45, v251, 29
	v_readlane_b32 s46, v251, 30
	v_readlane_b32 s47, v251, 31
	v_readlane_b32 s48, v251, 32
	v_readlane_b32 s49, v251, 33
	s_or_b32 s22, s14, s15
	s_mov_b64 s[14:15], 0

; DI void cvt_resolve(const CvtPtrs& P, int it, const float*& src, int& ldw, bf16_t*& dst, int& ldd, bool& qperm, bool& f8) {
;     ...
;     const int l = r / CVT_L, rr = r % CVT_L, kind = rr / 8192, q = rr % 8192, le = l * 16 + q / 512, rem = q % 512;
;     f8 = true;
;     if (kind < 2) { const int kt = ((rem >> 3) / 16) * 8 + (rem & 7), nt = (rem >> 3) % 16, n0 = nt * 64;
;         src = (kind ? P.wu : P.wg) + (size_t)le * DM * DFF + (size_t)(kt * 64) * DFF + n0; ldw = DFF;
;         dst = (bf16_t*)((unsigned char*)P.WGU + (size_t)(le * 2048 + (n0 >> 7) * 256 + kind * 128 + (n0 & 127)) * DM + kt * 64); ldd = DM; }
;     else { const int kt = ((rem >> 3) / 32) * 8 + (rem & 7), nt = (rem >> 3) % 32;
;         src = P.wd + (size_t)le * DFF * DM + (size_t)(kt * 64) * DM + nt * 64; ldw = DM; dst = (bf16_t*)((unsigned char*)P.WDN + (size_t)(le * 2048 + nt * 64) * DFF + kt * 64); ldd = DFF; }
.LBB0_869:
	s_and_b64 vcc, exec, s[16:17]
	s_cbranch_vccz .LBB0_871
	s_add_i32 s4, s39, 0x4280
	s_lshr_b32 s4, s4, 5
	s_and_b32 s4, s4, 0x3fffff8
	s_or_b32 s4, s4, s25
	s_lshl_b32 s4, s4, 6
	v_readlane_b32 s40, v251, 42
	s_lshl_b64 s[14:15], s[4:5], 13
	v_readlane_b32 s54, v251, 56
	v_readlane_b32 s55, v251, 57
	s_add_u32 s14, s54, s14
	s_addc_u32 s15, s55, s15
	s_and_b32 s16, s30, 0x7c0
	s_lshl_b32 s17, s16, 2
	s_add_u32 s20, s14, s17
	s_addc_u32 s21, s15, 0
	s_lshl_b32 s14, s16, 11
	v_readlane_b32 s15, v250, 5
	s_add_u32 s14, s15, s14
	v_readlane_b32 s15, v250, 6
	v_readlane_b32 s41, v251, 43
	s_addc_u32 s15, s15, 0
	v_readlane_b32 s40, v251, 60
	s_add_u32 s14, s14, s4
	v_readlane_b32 s41, v251, 61
	s_addc_u32 s15, s15, 0
	s_mov_b64 s[18:19], 0x800
	s_movk_i32 s4, 0x800
	v_readlane_b32 s42, v251, 44
	v_readlane_b32 s43, v251, 45
	v_readlane_b32 s44, v251, 46
	v_readlane_b32 s45, v251, 47
	v_readlane_b32 s46, v251, 48
	v_readlane_b32 s47, v251, 49
	v_readlane_b32 s48, v251, 50
	v_readlane_b32 s49, v251, 51
	v_readlane_b32 s50, v251, 52
	v_readlane_b32 s51, v251, 53
	v_readlane_b32 s52, v251, 54
	v_readlane_b32 s53, v251, 55

; DI void cvt_resolve(const CvtPtrs& P, int it, const float*& src, int& ldw, bf16_t*& dst, int& ldd, bool& qperm, bool& f8) {
;     ...
;     const int l = r / CVT_L, rr = r % CVT_L, kind = rr / 8192, q = rr % 8192, le = l * 16 + q / 512, rem = q % 512;
;     f8 = true;
;     if (kind < 2) { const int kt = ((rem >> 3) / 16) * 8 + (rem & 7), nt = (rem >> 3) % 16, n0 = nt * 64;
;         src = (kind ? P.wu : P.wg) + (size_t)le * DM * DFF + (size_t)(kt * 64) * DFF + n0; ldw = DFF;
;         dst = (bf16_t*)((unsigned char*)P.WGU + (size_t)(le * 2048 + (n0 >> 7) * 256 + kind * 128 + (n0 & 127)) * DM + kt * 64); ldd = DM; }
;     else { const int kt = ((rem >> 3) / 32) * 8 + (rem & 7), nt = (rem >> 3) % 32;
;         src = P.wd + (size_t)le * DFF * DM + (size_t)(kt * 64) * DM + nt * 64; ldw = DM; dst = (bf16_t*)((unsigned char*)P.WDN + (size_t)(le * 2048 + nt * 64) * DFF + kt * 64); ldd = DFF; }
.LBB0_874:
	s_andn2_b64 vcc, exec, s[22:23]
	s_cbranch_vccnz .LBB0_876
	s_addk_i32 s39, 0x4c80
	s_lshr_b32 s4, s39, 5
	s_and_b32 s4, s4, 0x3fffff8
	s_or_b32 s4, s4, s25
	s_lshl_b32 s4, s4, 6
	v_readlane_b32 s40, v251, 42
	s_lshl_b64 s[12:13], s[4:5], 13
	v_readlane_b32 s44, v251, 46
	v_readlane_b32 s45, v251, 47
	s_add_u32 s12, s44, s12
	s_addc_u32 s13, s45, s13
	s_and_b32 s14, s30, 0x7c0
	s_lshl_b32 s15, s14, 2
	s_add_u32 s20, s12, s15
	s_addc_u32 s21, s13, 0
	s_lshl_b32 s12, s14, 12
	v_readlane_b32 s13, v250, 2
	s_add_u32 s14, s13, s12
	v_readlane_b32 s41, v251, 43
	s_addc_u32 s15, s3, 0
	s_lshl_b64 s[12:13], s[4:5], 1
	v_readlane_b32 s40, v251, 60
	s_add_u32 s14, s14, s12
	v_readlane_b32 s41, v251, 61
	s_addc_u32 s15, s15, s13
	s_mov_b64 s[18:19], 0x800
	s_movk_i32 s4, 0x800
	s_mov_b64 s[12:13], 0
	s_mov_b64 s[16:17], 0
	v_readlane_b32 s42, v251, 44
	v_readlane_b32 s43, v251, 45
	v_readlane_b32 s46, v251, 48
	v_readlane_b32 s47, v251, 49
	v_readlane_b32 s48, v251, 50
	v_readlane_b32 s49, v251, 51
	v_readlane_b32 s50, v251, 52
	v_readlane_b32 s51, v251, 53
	v_readlane_b32 s52, v251, 54
	v_readlane_b32 s53, v251, 55
	v_readlane_b32 s54, v251, 56
	v_readlane_b32 s55, v251, 57

; #define LAS __attribute__((address_space(3)))
; DI void cvt_resolve(const CvtPtrs& P, int it, const float*& src, int& ldw, bf16_t*& dst, int& ldd, bool& qperm, bool& f8) {
;     ...
;     const int l = r / CVT_L, rr = r % CVT_L, kind = rr / 8192, q = rr % 8192, le = l * 16 + q / 512, rem = q % 512;
;     f8 = true;
;     if (kind < 2) { const int kt = ((rem >> 3) / 16) * 8 + (rem & 7), nt = (rem >> 3) % 16, n0 = nt * 64;
;         src = (kind ? P.wu : P.wg) + (size_t)le * DM * DFF + (size_t)(kt * 64) * DFF + n0; ldw = DFF;
;         dst = (bf16_t*)((unsigned char*)P.WGU + (size_t)(le * 2048 + (n0 >> 7) * 256 + kind * 128 + (n0 & 127)) * DM + kt * 64); ldd = DM; }
;     else { const int kt = ((rem >> 3) / 32) * 8 + (rem & 7), nt = (rem >> 3) % 32;
;         src = P.wd + (size_t)le * DFF * DM + (size_t)(kt * 64) * DM + nt * 64; ldw = DM; dst = (bf16_t*)((unsigned char*)P.WDN + (size_t)(le * 2048 + nt * 64) * DFF + kt * 64); ldd = DFF; }
; }
; DI void cvt_range(const CvtPtrs& P, int lo, int hi, int w, int NW, LAS unsigned* scr, int lane) {
;     int it = lo + w; if (it >= hi) return;
;     const int c = lane & 15, q = lane >> 4;
;     const float* src; int ldw; bf16_t* dst; int ldd; bool qperm, f8; cvt_resolve(P, it, src, ldw, dst, ldd, qperm, f8);
;     f32x4 v[16];
; #pragma unroll
;     for (int rr = 0; rr < 16; ++rr) v[rr] = __builtin_nontemporal_load((const f32x4*)(src + (size_t)(16 * q + rr) * ldw + 4 * c));
.LBB0_963:
	s_abs_i32 s7, s33
	v_cvt_f32_u32_e32 v2, s7
	s_add_i32 s6, s33, 0x47f
	s_xor_b32 s8, s6, s33
	s_abs_i32 s9, s6
	v_rcp_iflag_f32_e32 v2, v2
	s_sub_i32 s10, 0, s7
	s_ashr_i32 s6, s8, 31
	v_mul_f32_e32 v2, 0x4f7ffffe, v2
	v_cvt_u32_f32_e32 v2, v2
	s_nop 0
	v_readfirstlane_b32 s8, v2
	s_mul_i32 s10, s10, s8
	s_mul_hi_u32 s10, s8, s10
	s_add_i32 s8, s8, s10
	s_mul_hi_u32 s8, s9, s8
	s_mul_i32 s10, s8, s7
	s_sub_i32 s9, s9, s10
	s_add_i32 s11, s8, 1
	s_sub_i32 s10, s9, s7
	s_cmp_ge_u32 s9, s7
	s_cselect_b32 s8, s11, s8
	s_cselect_b32 s9, s10, s9
	s_add_i32 s10, s8, 1
	s_cmp_ge_u32 s9, s7
	s_cselect_b32 s7, s10, s8
	s_xor_b32 s10, s7, s6
	s_sub_i32 s11, s10, s6
	s_add_i32 s12, s11, -1
	s_mul_i32 s12, s12, s33
	s_sub_i32 s8, 0x480, s12
	s_cmp_lt_i32 s2, s8
	s_cbranch_scc1 .LBB0_1001
	s_sub_i32 s7, s2, s8
	s_lshl_b32 s7, s7, 3
	v_readlane_b32 s9, v251, 25
	s_add_i32 s7, s7, s9
	s_cmpk_gt_u32 s7, 0x67f
	s_cbranch_scc1 .LBB0_1001
	s_add_i32 s13, s7, 0x3640
	s_lshr_b32 s7, s13, 4
	s_sub_i32 s8, s33, s8
	s_bfe_u32 s27, s88, 0x30006
	s_lshr_b32 s14, s13, 9
	s_and_b32 s7, s7, 24
	v_readlane_b32 s16, v251, 28
	s_lshl_b32 s26, s8, 3
	s_or_b32 s7, s7, s27
	s_lshl_b32 s15, s13, 3
	s_lshl_b32 s8, s14, 23
	v_readlane_b32 s20, v251, 32
	v_readlane_b32 s21, v251, 33
	s_add_u32 s8, s20, s8
	s_addc_u32 s9, s21, 0
	s_lshl_b32 s16, s7, 6
	s_lshl_b32 s7, s7, 18
	s_add_u32 s7, s8, s7
	s_addc_u32 s9, s9, 0
	s_lshl_b32 s8, s13, 5
	s_and_b32 s8, s8, 0xf00
	v_and_b32_e32 v98, 48, v0
	v_and_b32_e32 v100, 60, v195
	v_mov_b32_e32 v103, 0
	s_add_u32 s8, s7, s8
	v_or_b32_e32 v104, 1, v98
	s_addc_u32 s9, s9, 0
	v_lshlrev_b32_e32 v26, 2, v100
	v_mov_b32_e32 v27, v103
	v_lshlrev_b32_e32 v102, 12, v98
	v_lshlrev_b32_e32 v2, 12, v104
	s_waitcnt lgkmcnt(0)
	v_mov_b32_e32 v3, v103
	v_or_b32_e32 v106, 2, v98
	v_lshl_add_u64 v[48:49], s[8:9], 0, v[26:27]
	v_lshlrev_b32_e32 v4, 12, v106
	v_mov_b32_e32 v5, v103
	v_or_b32_e32 v108, 3, v98
	v_or_b32_e32 v110, 4, v98
	v_lshl_add_u64 v[26:27], v[48:49], 0, v[102:103]
	v_lshl_add_u64 v[2:3], v[48:49], 0, v[2:3]
	v_lshlrev_b32_e32 v6, 12, v108
	v_mov_b32_e32 v7, v103
	v_lshlrev_b32_e32 v8, 12, v110
	v_mov_b32_e32 v9, v103
	v_or_b32_e32 v112, 5, v98
	v_or_b32_e32 v114, 6, v98
	global_load_dwordx4 v[26:29], v[26:27], off nt
	s_nop 0
	global_load_dwordx4 v[30:33], v[2:3], off nt
	v_lshl_add_u64 v[2:3], v[48:49], 0, v[4:5]
	v_lshlrev_b32_e32 v10, 12, v112
	v_mov_b32_e32 v11, v103
	v_lshlrev_b32_e32 v12, 12, v114
	v_mov_b32_e32 v13, v103
	v_or_b32_e32 v116, 7, v98
	v_or_b32_e32 v118, 8, v98
	v_lshl_add_u64 v[4:5], v[48:49], 0, v[6:7]
	global_load_dwordx4 v[38:41], v[2:3], off nt
	global_load_dwordx4 v[42:45], v[4:5], off nt
	v_lshl_add_u64 v[2:3], v[48:49], 0, v[8:9]
	v_lshlrev_b32_e32 v14, 12, v116
	v_mov_b32_e32 v15, v103
	v_lshlrev_b32_e32 v16, 12, v118
	v_mov_b32_e32 v17, v103
	v_or_b32_e32 v120, 9, v98
	v_or_b32_e32 v122, 10, v98
	v_lshl_add_u64 v[4:5], v[48:49], 0, v[10:11]
	global_load_dwordx4 v[50:53], v[2:3], off nt
	global_load_dwordx4 v[54:57], v[4:5], off nt
	v_lshl_add_u64 v[2:3], v[48:49], 0, v[12:13]
	v_lshlrev_b32_e32 v18, 12, v120
	v_mov_b32_e32 v19, v103
	v_lshlrev_b32_e32 v20, 12, v122
	v_mov_b32_e32 v21, v103
	v_or_b32_e32 v124, 11, v98
	v_or_b32_e32 v126, 12, v98
	v_lshl_add_u64 v[4:5], v[48:49], 0, v[14:15]
	global_load_dwordx4 v[58:61], v[2:3], off nt
	global_load_dwordx4 v[62:65], v[4:5], off nt
	v_lshl_add_u64 v[2:3], v[48:49], 0, v[16:17]
	v_lshlrev_b32_e32 v22, 12, v124
	v_mov_b32_e32 v23, v103
	v_lshlrev_b32_e32 v24, 12, v126
	v_mov_b32_e32 v25, v103
	v_or_b32_e32 v128, 13, v98
	v_or_b32_e32 v130, 14, v98
	v_lshl_add_u64 v[4:5], v[48:49], 0, v[18:19]
	global_load_dwordx4 v[66:69], v[2:3], off nt
	global_load_dwordx4 v[70:73], v[4:5], off nt
	v_lshl_add_u64 v[2:3], v[48:49], 0, v[20:21]
	v_lshlrev_b32_e32 v34, 12, v128
	v_mov_b32_e32 v35, v103
	v_lshlrev_b32_e32 v36, 12, v130
	v_mov_b32_e32 v37, v103
	v_or_b32_e32 v132, 15, v194
	v_lshl_add_u64 v[4:5], v[48:49], 0, v[22:23]
	global_load_dwordx4 v[74:77], v[2:3], off nt
	global_load_dwordx4 v[78:81], v[4:5], off nt
	v_lshl_add_u64 v[2:3], v[48:49], 0, v[24:25]
	v_lshlrev_b32_e32 v46, 12, v132
	v_mov_b32_e32 v47, v103
	v_lshl_add_u64 v[4:5], v[48:49], 0, v[34:35]
	global_load_dwordx4 v[82:85], v[2:3], off nt
	global_load_dwordx4 v[86:89], v[4:5], off nt
	v_lshl_add_u64 v[2:3], v[48:49], 0, v[36:37]
	v_lshl_add_u64 v[4:5], v[48:49], 0, v[46:47]
	global_load_dwordx4 v[90:93], v[2:3], off nt
	global_load_dwordx4 v[94:97], v[4:5], off nt
	v_lshlrev_b32_e32 v2, 3, v0
	v_and_b32_e32 v1, 4, v1
	v_and_or_b32 v1, v2, 56, v1
	v_lshlrev_b32_e32 v2, 1, v0
	v_and_b32_e32 v2, 0x60, v2
	v_readlane_b32 s8, v250, 3
	s_lshl_b32 s9, s13, 4
	s_and_b32 s9, s9, 0x700
	v_add_u32_e32 v99, s8, v2
	v_and_b32_e32 v2, 7, v0
	v_lshl_add_u32 v3, v2, 4, s8
	v_add_u32_e32 v101, s8, v98
	v_add_u32_e32 v4, s8, v196
	s_lshl_b32 s8, s14, 11
	s_or_b32 s8, s8, s9
	s_and_b32 s9, s15, 64
	s_or_b32 s8, s8, s9
	s_lshl_b32 s8, s8, 11
	v_readlane_b32 s9, v250, 7
	s_add_u32 s8, s9, s8
	v_readlane_b32 s9, v250, 8
	s_addc_u32 s9, s9, 0
	s_add_u32 s8, s8, s16
	s_addc_u32 s9, s9, 0
	s_add_u32 s8, s8, 0x40000
	v_readlane_b32 s14, v251, 25
	s_addc_u32 s9, s9, 0
	s_lshl_b32 s28, s12, 9
	s_lshl_b32 s12, s2, 9
	s_lshl_b32 s13, s14, 6
	s_add_i32 s29, s12, s13
	s_lshl_b32 s12, s10, 4
	s_lshl_b32 s13, s6, 4
	s_sub_i32 s12, s12, s13
	s_add_i32 s12, s12, -8
	s_lshl_b32 s10, s10, 3
	s_lshl_b32 s6, s6, 3
	s_mul_i32 s12, s33, s12
	s_sub_i32 s6, s10, s6
	s_add_i32 s31, s14, s12
	s_add_i32 s6, s6, -8
	v_lshrrev_b32_e32 v134, 3, v194
	v_lshrrev_b32_e32 v150, 2, v194
	s_mul_i32 s11, s33, s11
	s_add_i32 s13, s31, s85
	s_mul_i32 s6, s33, s6
	v_lshlrev_b32_e32 v2, 3, v2
	v_mul_u32_u24_e32 v5, 0x90, v134
	v_mul_u32_u24_e32 v6, 0x50, v150
	s_lshl_b32 s30, s11, 9
	s_lshl_b32 s13, s13, 3
	s_lshl_b32 s35, s11, 6
	s_lshl_b32 s36, s12, 6
	s_add_i32 s6, s14, s6
	s_mov_b32 s7, 0
	v_mov_b32_e32 v197, v103
	v_or_b32_e32 v136, 8, v134
	v_or_b32_e32 v138, 16, v134
	v_or_b32_e32 v140, 24, v134
	v_or_b32_e32 v142, 32, v134
	v_or_b32_e32 v144, 40, v134
	v_or_b32_e32 v146, 48, v134
	v_or_b32_e32 v148, 56, v134
	v_or_b32_e32 v152, 16, v150
	v_or_b32_e32 v154, 32, v150
	v_or_b32_e32 v156, 48, v150
	s_add_i32 s28, s28, 0x231000
	s_add_i32 s30, s30, 0xfff70000
	s_add_i32 s34, s13, 0x34200
	s_add_i32 s35, s35, 0xfffee000
	s_add_i32 s36, s36, 0x1a1000
	s_add_i32 s37, s6, 0x8c40
	s_mov_b64 s[12:13], -1
	s_mov_b64 s[10:11], 0
	s_movk_i32 s39, 0x800
	s_mov_b32 s38, 0xc3e00000
	v_lshlrev_b32_e32 v158, 1, v2
	v_add_u32_e32 v105, v3, v5
	v_add_u32_e32 v107, v4, v6
	v_mov_b32_e32 v109, 0x43e00000
	v_readlane_b32 s17, v251, 29
	v_readlane_b32 s18, v251, 30
	v_readlane_b32 s19, v251, 31
	v_readlane_b32 s22, v251, 34
	v_readlane_b32 s23, v251, 35
	s_branch .LBB0_967

; DI void cvt_resolve(const CvtPtrs& P, int it, const float*& src, int& ldw, bf16_t*& dst, int& ldd, bool& qperm, bool& f8) {
;     int r = it; qperm = false; f8 = false;
;     if (r < 3072) { const int kt = ((r >> 3) / 96) * 8 + (r & 7), nt = (r >> 3) % 96, n0 = nt * 64, part = n0 >> 11, j0 = n0 & 2047;
;         src = P.cin + (size_t)(kt * 64) * 6144 + n0; ldw = 6144; ldd = DM;
;         dst = (part == 0 ? P.W1B + (size_t)j0 * DM : P.W1A + (size_t)((j0 >> 7) * 256 + (part == 2 ? 128 : 0) + (j0 & 127)) * DM) + kt * 64; return; } r -= 3072;
;     if (r < 1024) { const int kt = ((r >> 3) / 32) * 8 + (r & 7), nt = (r >> 3) % 32; src = P.cout + (size_t)(kt * 64) * DM + nt * 64; ldw = DM; dst = P.W2 + (size_t)(nt * 64) * DM + kt * 64; ldd = DM; return; } r -= 1024;
;     if (r < 1536) { const int kt = ((r >> 3) / 48) * 8 + (r & 7), nt = (r >> 3) % 48; src = P.wqkv + (size_t)(kt * 64) * 3072 + nt * 64; ldw = 3072; qperm = nt < 40;     f8 = true; dst = (bf16_t*)((unsigned char*)P.WQKV + (size_t)(nt * 64) * DM + kt * 64); ldd = DM;     return; } r -= 1536;
;     if (r < 1024) { const int kt = ((r >> 3) / 32) * 8 + (r & 7), nt = (r >> 3) % 32; src = P.wo + (size_t)(kt * 64) * DM + nt * 64; ldw = DM; f8 = true;
;         dst = (bf16_t*)((unsigned char*)P.WO + (size_t)(nt * 64) * DM + kt * 64); ldd = DM; return; } r -= 1024;
;     const int l = r / CVT_L, rr = r % CVT_L, kind = rr / 8192, q = rr % 8192, le = l * 16 + q / 512, rem = q % 512;
;     f8 = true;
;     if (kind < 2) { const int kt = ((rem >> 3) / 16) * 8 + (rem & 7), nt = (rem >> 3) % 16, n0 = nt * 64;
;         src = (kind ? P.wu : P.wg) + (size_t)le * DM * DFF + (size_t)(kt * 64) * DFF + n0; ldw = DFF;
;         dst = (bf16_t*)((unsigned char*)P.WGU + (size_t)(le * 2048 + (n0 >> 7) * 256 + kind * 128 + (n0 & 127)) * DM + kt * 64); ldd = DM; }
;     else { const int kt = ((rem >> 3) / 32) * 8 + (rem & 7), nt = (rem >> 3) % 32;
;         src = P.wd + (size_t)le * DFF * DM + (size_t)(kt * 64) * DM + nt * 64; ldw = DM; dst = (bf16_t*)((unsigned char*)P.WDN + (size_t)(le * 2048 + nt * 64) * DFF + kt * 64); ldd = DFF; }
; }
.LBB0_971:
	s_add_i32 s57, s85, s31
	s_add_i32 s56, s57, 0x6840
	s_cmp_gt_i32 s56, 0xb6bf
	s_mov_b64 s[14:15], s[12:13]
	s_mov_b64 s[18:19], s[10:11]
	s_mov_b32 s6, s39
	s_mov_b64 s[16:17], s[8:9]
	s_cbranch_scc1 .LBB0_997
	s_cmpk_gt_i32 s56, 0xbff
	s_mov_b64 s[24:25], -1
	s_cbranch_scc0 .LBB0_990
	s_mov_b64 s[14:15], -1
	s_cmpk_gt_u32 s56, 0xfff
	s_cbranch_scc0 .LBB0_987
	s_cmpk_gt_u32 s56, 0x15ff
	s_mov_b64 s[18:19], -1
	s_cbranch_scc0 .LBB0_985
	s_cmpk_gt_u32 s56, 0x19ff
	s_cbranch_scc0 .LBB0_982
	s_add_i32 s16, s57, 0x4e40
	s_add_i32 s6, s57, 0xffffee40
	s_cmpk_lt_u32 s16, 0x6000
	s_cselect_b32 s6, s16, s6
	s_cmpk_gt_u32 s16, 0x5fff
	s_cselect_b32 s16, 16, 0
	s_bfe_u32 s17, s6, 0x40009
	s_or_b32 s19, s17, s16
	s_and_b32 s20, s6, 7
	s_mov_b32 s25, s88
	s_cmpk_gt_u32 s6, 0x3fff
	s_mov_b64 s[16:17], -1
	s_cbranch_scc0 .LBB0_978
	s_lshr_b32 s16, s6, 5
	s_and_b32 s16, s16, 8
	v_readlane_b32 s44, v251, 28
	s_or_b32 s16, s16, s20
	s_lshl_b32 s17, s19, 23
	v_readlane_b32 s50, v251, 34
	v_readlane_b32 s51, v251, 35
	s_add_u32 s17, s50, s17
	s_addc_u32 s21, s51, 0
	s_lshl_b32 s18, s16, 6
	s_lshl_b32 s16, s16, 19
	s_add_u32 s16, s17, s16
	s_addc_u32 s17, s21, 0
	s_lshl_b32 s21, s6, 3
	s_and_b32 s21, s21, 0x7c0
	s_lshl_b32 s22, s21, 2
	s_add_u32 s22, s16, s22
	s_addc_u32 s23, s17, 0
	s_lshl_b32 s16, s19, 21
	s_lshl_b32 s17, s21, 10
	v_readlane_b32 s45, v251, 29
	v_readlane_b32 s46, v251, 30
	v_readlane_b32 s47, v251, 31
	v_readlane_b32 s48, v251, 32
	v_readlane_b32 s49, v251, 33
	s_or_b32 s24, s16, s17
	s_mov_b64 s[16:17], 0

; DI void cvt_resolve(const CvtPtrs& P, int it, const float*& src, int& ldw, bf16_t*& dst, int& ldd, bool& qperm, bool& f8) {
;     ...
;     const int l = r / CVT_L, rr = r % CVT_L, kind = rr / 8192, q = rr % 8192, le = l * 16 + q / 512, rem = q % 512;
;     f8 = true;
;     if (kind < 2) { const int kt = ((rem >> 3) / 16) * 8 + (rem & 7), nt = (rem >> 3) % 16, n0 = nt * 64;
;         src = (kind ? P.wu : P.wg) + (size_t)le * DM * DFF + (size_t)(kt * 64) * DFF + n0; ldw = DFF;
;         dst = (bf16_t*)((unsigned char*)P.WGU + (size_t)(le * 2048 + (n0 >> 7) * 256 + kind * 128 + (n0 & 127)) * DM + kt * 64); ldd = DM; }
;     else { const int kt = ((rem >> 3) / 32) * 8 + (rem & 7), nt = (rem >> 3) % 32;
;         src = P.wd + (size_t)le * DFF * DM + (size_t)(kt * 64) * DM + nt * 64; ldw = DM; dst = (bf16_t*)((unsigned char*)P.WDN + (size_t)(le * 2048 + nt * 64) * DFF + kt * 64); ldd = DFF; }
.LBB0_982:
	s_and_b64 vcc, exec, s[18:19]
	s_cbranch_vccz .LBB0_984
	s_add_i32 s6, s57, 0x5240
	s_lshr_b32 s6, s6, 5
	s_and_b32 s6, s6, 0x3fffff8
	s_or_b32 s6, s6, s27
	s_lshl_b32 s6, s6, 6
	v_readlane_b32 s40, v251, 42
	s_lshl_b64 s[16:17], s[6:7], 13
	v_readlane_b32 s54, v251, 56
	v_readlane_b32 s55, v251, 57
	s_add_u32 s16, s54, s16
	s_addc_u32 s17, s55, s17
	s_and_b32 s18, s34, 0x7c0
	s_lshl_b32 s19, s18, 2
	s_add_u32 s22, s16, s19
	s_addc_u32 s23, s17, 0
	s_lshl_b32 s16, s18, 11
	v_readlane_b32 s17, v250, 5
	s_add_u32 s16, s17, s16
	v_readlane_b32 s17, v250, 6
	v_readlane_b32 s41, v251, 43
	s_addc_u32 s17, s17, 0
	v_readlane_b32 s40, v251, 60
	v_readlane_b32 s96, v251, 36
	s_add_u32 s16, s16, s6
	v_readlane_b32 s41, v251, 61
	v_readlane_b32 s97, v251, 37
	s_addc_u32 s17, s17, 0
	s_mov_b64 s[20:21], 0x800
	s_movk_i32 s6, 0x800
	v_readlane_b32 s42, v251, 44
	v_readlane_b32 s43, v251, 45
	v_readlane_b32 s44, v251, 46
	v_readlane_b32 s45, v251, 47
	v_readlane_b32 s46, v251, 48
	v_readlane_b32 s47, v251, 49
	v_readlane_b32 s48, v251, 50
	v_readlane_b32 s49, v251, 51
	v_readlane_b32 s50, v251, 52
	v_readlane_b32 s51, v251, 53
	v_readlane_b32 s52, v251, 54
	v_readlane_b32 s53, v251, 55

; DI void cvt_resolve(const CvtPtrs& P, int it, const float*& src, int& ldw, bf16_t*& dst, int& ldd, bool& qperm, bool& f8) {
;     ...
;     const int l = r / CVT_L, rr = r % CVT_L, kind = rr / 8192, q = rr % 8192, le = l * 16 + q / 512, rem = q % 512;
;     f8 = true;
;     if (kind < 2) { const int kt = ((rem >> 3) / 16) * 8 + (rem & 7), nt = (rem >> 3) % 16, n0 = nt * 64;
;         src = (kind ? P.wu : P.wg) + (size_t)le * DM * DFF + (size_t)(kt * 64) * DFF + n0; ldw = DFF;
;         dst = (bf16_t*)((unsigned char*)P.WGU + (size_t)(le * 2048 + (n0 >> 7) * 256 + kind * 128 + (n0 & 127)) * DM + kt * 64); ldd = DM; }
;     else { const int kt = ((rem >> 3) / 32) * 8 + (rem & 7), nt = (rem >> 3) % 32;
;         src = P.wd + (size_t)le * DFF * DM + (size_t)(kt * 64) * DM + nt * 64; ldw = DM; dst = (bf16_t*)((unsigned char*)P.WDN + (size_t)(le * 2048 + nt * 64) * DFF + kt * 64); ldd = DFF; }
.LBB0_987:
	s_andn2_b64 vcc, exec, s[24:25]
	s_cbranch_vccnz .LBB0_989
	s_addk_i32 s57, 0x5c40
	s_lshr_b32 s6, s57, 5
	s_and_b32 s6, s6, 0x3fffff8
	s_or_b32 s6, s6, s27
	s_lshl_b32 s6, s6, 6
	v_readlane_b32 s40, v251, 42
	s_lshl_b64 s[14:15], s[6:7], 13
	v_readlane_b32 s44, v251, 46
	v_readlane_b32 s45, v251, 47
	s_add_u32 s14, s44, s14
	s_addc_u32 s15, s45, s15
	s_and_b32 s16, s34, 0x7c0
	s_lshl_b32 s17, s16, 2
	s_add_u32 s22, s14, s17
	s_addc_u32 s23, s15, 0
	s_lshl_b32 s14, s16, 12
	v_readlane_b32 s15, v250, 2
	s_add_u32 s16, s15, s14
	v_readlane_b32 s41, v251, 43
	s_addc_u32 s17, s3, 0
	s_lshl_b64 s[14:15], s[6:7], 1
	v_readlane_b32 s40, v251, 60
	v_readlane_b32 s96, v251, 36
	s_add_u32 s16, s16, s14
	v_readlane_b32 s41, v251, 61
	v_readlane_b32 s97, v251, 37
	s_addc_u32 s17, s17, s15
	s_mov_b64 s[20:21], 0x800
	s_movk_i32 s6, 0x800
	s_mov_b64 s[14:15], 0
	s_mov_b64 s[18:19], 0
	v_readlane_b32 s42, v251, 44
	v_readlane_b32 s43, v251, 45
	v_readlane_b32 s46, v251, 48
	v_readlane_b32 s47, v251, 49
	v_readlane_b32 s48, v251, 50
	v_readlane_b32 s49, v251, 51
	v_readlane_b32 s50, v251, 52
	v_readlane_b32 s51, v251, 53
	v_readlane_b32 s52, v251, 54
	v_readlane_b32 s53, v251, 55
	v_readlane_b32 s54, v251, 56
	v_readlane_b32 s55, v251, 57
